# row phases: next row's X prefetched during the current row (4 phases) + permlane-swap wave reduction
# baseline (speedup 1.0000x reference)
.LBB0_673:
	s_cmp_lt_i32 s92, 8
	s_cselect_b64 s[4:5], -1, 0
	s_cmp_gt_i32 s93, 7
	s_cselect_b64 s[6:7], -1, 0
	s_and_b64 s[4:5], s[4:5], s[6:7]
	s_andn2_b64 vcc, exec, s[4:5]
	s_cbranch_vccnz .LBB0_729
	s_lshl_b32 s3, s89, 3
	s_add_i32 s6, s3, s88
	s_cmpk_gt_i32 s6, 0x43ff
	s_mov_b32 s4, 7
	s_cbranch_scc1 .LBB0_679
	s_ashr_i32 s5, s4, 31
	s_lshl_b32 s8, s34, 3
	s_lshl_b64 s[4:5], s[4:5], 3
	s_add_u32 s4, s0, s4
	s_addc_u32 s5, s1, s5
	s_load_dwordx2 s[4:5], s[4:5], 0x0
	s_waitcnt vmcnt(0)
	v_lshlrev_b32_e32 v18, 2, v250
	v_ashrrev_i32_e32 v19, 31, v18
	v_lshlrev_b64 v[20:21], 2, v[18:19]
	v_mbcnt_lo_u32_b32 v1, -1, 0
	s_waitcnt lgkmcnt(0)
	v_lshl_add_u64 v[22:23], s[4:5], 0, v[20:21]
	global_load_dwordx4 v[2:5], v[22:23], off
	global_load_dwordx4 v[6:9], v[22:23], off offset:1024
	global_load_dwordx4 v[10:13], v[22:23], off offset:2048
	global_load_dwordx4 v[14:17], v[22:23], off offset:3072
	v_mbcnt_hi_u32_b32 v22, -1, v1
	v_and_b32_e32 v23, 64, v22
	v_xor_b32_e32 v1, 16, v22
	v_add_u32_e32 v23, 64, v23
	v_cmp_lt_i32_e32 vcc, v1, v23
	v_xor_b32_e32 v24, 32, v22
	v_lshl_add_u64 v[20:21], s[26:27], 0, v[20:21]
	v_cndmask_b32_e32 v1, v22, v1, vcc
	v_cmp_lt_i32_e32 vcc, v24, v23
	s_mov_b64 s[4:5], 0x103000
	s_ashr_i32 s7, s6, 31
	v_cndmask_b32_e32 v22, v22, v24, vcc
	v_lshlrev_b32_e32 v92, 2, v22
	v_lshl_add_u64 v[22:23], v[20:21], 0, s[4:5]
	s_mov_b64 s[4:5], 0x104000
	v_lshl_add_u64 v[24:25], v[20:21], 0, s[4:5]
	s_mov_b64 s[4:5], 0x11a000
	v_lshl_add_u64 v[26:27], v[20:21], 0, s[4:5]
	s_lshl_b64 s[4:5], s[6:7], 11
	s_add_u32 s4, s26, s4
	s_addc_u32 s5, s27, s5
	v_lshl_add_u64 v[18:19], v[18:19], 1, s[4:5]
	s_mov_b64 s[4:5], 0x3e500600
	s_ashr_i32 s9, s8, 31
	s_mov_b32 s14, 0xdd1ffa00
	s_mov_b32 s16, 0xdd1ffc00
	s_mov_b32 s18, 0xdd1ffe00
	s_mov_b32 s20, 0xdd200000
	s_mov_b32 s11, 0
	v_lshlrev_b32_e32 v1, 2, v1
	v_lshl_add_u64 v[28:29], v[18:19], 0, s[4:5]
	s_lshl_b64 s[12:13], s[8:9], 11
	s_mov_b32 s15, -1
	s_mov_b32 s3, 0xffff0000
	s_mov_b32 s17, -1
	s_mov_b32 s19, -1
	s_mov_b32 s21, -1
	s_mov_b32 s7, 0xff400000
	s_mov_b32 s9, 0xff600000
	s_mov_b32 s22, 0xff800000
	s_mov_b32 s23, 0xffa00000
	s_mov_b32 s30, 0xffc00000
	s_mov_b32 s31, 0xffe00000
	s_movk_i32 s33, 0x7fff
	v_mov_b32_e32 v93, 0x358637bd
	s_mov_b32 s35, 0xf800000
	v_mov_b32_e32 v94, 0x260
	s_mov_b32 s36, 0xe1600000
	v_mov_b32_e32 v95, 1
	v_add_co_u32_e32 v112, vcc, 0xdd200000, v28
	s_nop 1
	v_addc_co_u32_e32 v113, vcc, -1, v29, vcc
	global_load_dwordx2 v[114:115], v[112:113], off offset:-1536
	global_load_dwordx2 v[116:117], v[112:113], off offset:-1024
	global_load_dwordx2 v[118:119], v[112:113], off offset:-512
	global_load_dwordx2 v[120:121], v[112:113], off
	s_waitcnt vmcnt(0)
	s_branch .LBB0_677
.LBB0_676:
	s_add_i32 s10, s6, 0xfffffc00
	s_lshr_b32 s10, s10, 12
	s_mulk_i32 s10, 0x1800
	s_and_b64 s[4:5], s[4:5], exec
	s_cselect_b32 s10, 0x6000, s10
	s_lshl_b64 s[4:5], s[10:11], 2
	v_pk_mul_f32 v[62:63], v[32:33], v[32:33]
	v_pk_mul_f32 v[64:65], v[30:31], v[30:31]
	v_lshl_add_u64 v[66:67], v[24:25], 0, s[4:5]
	v_pk_mul_f32 v[58:59], v[34:35], v[34:35]
	v_pk_mul_f32 v[60:61], v[44:45], v[44:45]
	global_load_dwordx4 v[18:21], v[66:67], off
	global_load_dwordx4 v[46:49], v[66:67], off offset:1024
	global_load_dwordx4 v[50:53], v[66:67], off offset:2048
	global_load_dwordx4 v[54:57], v[66:67], off offset:3072
	v_pk_mov_b32 v[66:67], v[64:65], v[62:63] op_sel:[1,0]
	v_mov_b32_e32 v65, v63
	v_pk_add_f32 v[62:63], v[66:67], v[64:65]
	v_pk_mov_b32 v[64:65], v[60:61], v[58:59] op_sel:[1,0]
	v_mov_b32_e32 v61, v59
	v_pk_add_f32 v[58:59], v[64:65], v[60:61]
	v_pk_add_f32 v[62:63], v[62:63], v[62:63] op_sel_hi:[0,1]
	v_pk_add_f32 v[58:59], v[58:59], v[58:59] op_sel_hi:[0,1]
	v_mul_f32_e32 v58, v42, v42
	v_pk_fma_f32 v[60:61], v[42:43], v[42:43], v[58:59] op_sel_hi:[1,1,0]
	v_mul_f32_e32 v58, v36, v36
	v_pk_fma_f32 v[64:65], v[36:37], v[36:37], v[58:59] op_sel_hi:[1,1,0]
	v_mul_f32_e32 v60, v38, v38
	v_mul_f32_e32 v64, v39, v39
	v_mul_f32_e32 v62, v40, v40
	v_mul_f32_e32 v58, v41, v41
	v_pk_add_f32 v[66:67], v[60:61], v[64:65]
	v_pk_add_f32 v[68:69], v[62:63], v[58:59]
	v_lshl_add_u64 v[74:75], v[22:23], 0, s[4:5]
	v_pk_add_f32 v[66:67], v[66:67], v[68:69]
	global_load_dwordx4 v[58:61], v[74:75], off offset:2048
	global_load_dwordx4 v[62:65], v[74:75], off offset:3072
	v_add_f32_e32 v76, v66, v67
	global_load_dwordx4 v[66:69], v[74:75], off
	global_load_dwordx4 v[70:73], v[74:75], off offset:1024
	v_lshl_add_u64 v[112:113], v[112:113], 0, s[12:13]
	global_load_dwordx2 v[114:115], v[112:113], off offset:-1536
	global_load_dwordx2 v[116:117], v[112:113], off offset:-1024
	global_load_dwordx2 v[118:119], v[112:113], off offset:-512
	global_load_dwordx2 v[120:121], v[112:113], off
	v_add_f32_dpp v74, v76, v76 row_ror:8 row_mask:0xf bank_mask:0xf bound_ctrl:1
	s_add_i32 s6, s6, s8
	s_cmpk_lt_i32 s6, 0x4400
	v_add_f32_dpp v74, v74, v74 row_ror:4 row_mask:0xf bank_mask:0xf bound_ctrl:1
	s_waitcnt vmcnt(11)
	v_pk_add_f32 v[18:19], v[18:19], 1.0 op_sel_hi:[1,0]
	v_add_f32_dpp v74, v74, v74 row_ror:2 row_mask:0xf bank_mask:0xf bound_ctrl:1
	v_pk_add_f32 v[20:21], v[20:21], 1.0 op_sel_hi:[1,0]
	s_waitcnt vmcnt(10)
	v_pk_add_f32 v[46:47], v[46:47], 1.0 op_sel_hi:[1,0]
	v_add_f32_dpp v74, v74, v74 row_ror:1 row_mask:0xf bank_mask:0xf bound_ctrl:1
	v_mov_b32_e32 v75, v74
	s_nop 1
	v_permlane16_swap_b32_e32 v74, v75
	v_pk_add_f32 v[48:49], v[48:49], 1.0 op_sel_hi:[1,0]
	s_waitcnt vmcnt(9)
	v_pk_add_f32 v[50:51], v[50:51], 1.0 op_sel_hi:[1,0]
	v_pk_add_f32 v[52:53], v[52:53], 1.0 op_sel_hi:[1,0]
	s_waitcnt vmcnt(8)
	v_pk_add_f32 v[54:55], v[54:55], 1.0 op_sel_hi:[1,0]
	s_waitcnt lgkmcnt(0)
	v_add_f32_e32 v74, v74, v75
	v_mov_b32_e32 v75, v74
	s_nop 1
	v_permlane32_swap_b32_e32 v74, v75
	v_pk_add_f32 v[56:57], v[56:57], 1.0 op_sel_hi:[1,0]
	s_waitcnt lgkmcnt(0)
	v_add_f32_e32 v74, v74, v75
	v_fmamk_f32 v74, v74, 0x3a800000, v93
	v_mul_f32_e32 v75, 0x4f800000, v74
	v_cmp_gt_f32_e32 vcc, s35, v74
	s_nop 1
	v_cndmask_b32_e32 v74, v74, v75, vcc
	v_sqrt_f32_e32 v75, v74
	s_nop 0
	v_add_u32_e32 v76, -1, v75
	v_add_u32_e32 v77, 1, v75
	v_fma_f32 v78, -v76, v75, v74
	v_fma_f32 v79, -v77, v75, v74
	v_cmp_ge_f32_e64 s[4:5], 0, v78
	s_nop 1
	v_cndmask_b32_e64 v75, v75, v76, s[4:5]
	v_cmp_lt_f32_e64 s[4:5], 0, v79
	s_nop 1
	v_cndmask_b32_e64 v75, v75, v77, s[4:5]
	v_mul_f32_e32 v76, 0x37800000, v75
	v_cndmask_b32_e32 v75, v75, v76, vcc
	v_cmp_class_f32_e32 vcc, v74, v94
	s_nop 1
	v_cndmask_b32_e32 v74, v75, v74, vcc
	v_div_scale_f32 v75, s[4:5], v74, v74, 1.0
	v_rcp_f32_e32 v76, v75
	v_div_scale_f32 v77, vcc, 1.0, v74, 1.0
	v_fma_f32 v78, -v75, v76, 1.0
	v_fmac_f32_e32 v76, v78, v76
	v_mul_f32_e32 v78, v77, v76
	v_fma_f32 v79, -v75, v78, v77
	v_fmac_f32_e32 v78, v79, v76
	v_fma_f32 v75, -v75, v78, v77
	v_div_fmas_f32 v75, v75, v76, v78
	v_div_fixup_f32 v74, v75, v74, 1.0
	v_pk_mul_f32 v[30:31], v[30:31], v[74:75] op_sel_hi:[1,0]
	v_pk_mul_f32 v[32:33], v[32:33], v[74:75] op_sel_hi:[1,0]
	v_pk_mul_f32 v[30:31], v[2:3], v[30:31]
	v_pk_mul_f32 v[32:33], v[4:5], v[32:33]
	s_waitcnt vmcnt(5)
	v_pk_fma_f32 v[18:19], v[18:19], v[30:31], v[66:67]
	v_pk_fma_f32 v[20:21], v[20:21], v[32:33], v[68:69]
	v_bfe_u32 v30, v18, 16, 1
	v_add3_u32 v18, v18, v30, s33
	v_bfe_u32 v30, v19, 16, 1
	v_lshrrev_b32_e32 v18, 16, v18
	v_add3_u32 v19, v19, v30, s33
	v_and_or_b32 v18, v19, s3, v18
	v_bfe_u32 v19, v20, 16, 1
	v_add3_u32 v19, v20, v19, s33
	v_bfe_u32 v20, v21, 16, 1
	v_pk_mul_f32 v[44:45], v[44:45], v[74:75] op_sel_hi:[1,0]
	v_lshrrev_b32_e32 v19, 16, v19
	v_add3_u32 v20, v21, v20, s33
	v_pk_mul_f32 v[44:45], v[6:7], v[44:45]
	v_and_or_b32 v19, v20, s3, v19
	v_add_co_u32_e32 v20, vcc, s36, v28
	s_waitcnt vmcnt(4)
	v_pk_fma_f32 v[44:45], v[46:47], v[44:45], v[70:71]
	v_addc_co_u32_e32 v21, vcc, -1, v29, vcc
	v_pk_mul_f32 v[34:35], v[34:35], v[74:75] op_sel_hi:[1,0]
	global_store_dwordx2 v[20:21], v[18:19], off offset:-1536
	v_pk_mul_f32 v[34:35], v[8:9], v[34:35]
	v_pk_fma_f32 v[34:35], v[48:49], v[34:35], v[72:73]
	v_cvt_pk_bf16_f32 v18, v44, v45
	v_pk_mul_f32 v[42:43], v[42:43], v[74:75] op_sel_hi:[1,0]
	v_pk_mul_f32 v[42:43], v[10:11], v[42:43]
	v_pk_fma_f32 v[42:43], v[50:51], v[42:43], v[58:59]
	v_cvt_pk_bf16_f32 v19, v34, v35
	v_pk_mul_f32 v[36:37], v[36:37], v[74:75] op_sel_hi:[1,0]
	global_store_dwordx2 v[20:21], v[18:19], off offset:-1024
	v_pk_mul_f32 v[36:37], v[12:13], v[36:37]
	v_pk_fma_f32 v[36:37], v[52:53], v[36:37], v[60:61]
	v_cvt_pk_bf16_f32 v18, v42, v43
	v_pk_mul_f32 v[38:39], v[38:39], v[74:75] op_sel_hi:[1,0]
	v_pk_mul_f32 v[38:39], v[14:15], v[38:39]
	v_pk_fma_f32 v[38:39], v[54:55], v[38:39], v[62:63]
	v_cvt_pk_bf16_f32 v19, v36, v37
	v_pk_mul_f32 v[40:41], v[40:41], v[74:75] op_sel_hi:[1,0]
	global_store_dwordx2 v[20:21], v[18:19], off offset:-512
	v_pk_mul_f32 v[40:41], v[16:17], v[40:41]
	v_pk_fma_f32 v[40:41], v[56:57], v[40:41], v[64:65]
	v_cvt_pk_bf16_f32 v18, v38, v39
	v_cvt_pk_bf16_f32 v19, v40, v41
	v_lshl_add_u64 v[28:29], v[28:29], 0, s[12:13]
	global_store_dwordx2 v[20:21], v[18:19], off
	s_cbranch_scc0 .LBB0_679
.LBB0_677:
	s_waitcnt vmcnt(4)
	s_cmpk_lt_i32 s6, 0x400
	s_cselect_b64 s[4:5], -1, 0
	s_cmpk_gt_i32 s6, 0x3ff
	v_lshlrev_b32_e32 v30, 16, v114
	v_and_b32_e32 v31, 0xffff0000, v114
	v_lshlrev_b32_e32 v32, 16, v115
	v_and_b32_e32 v33, 0xffff0000, v115
	v_lshlrev_b32_e32 v44, 16, v116
	v_and_b32_e32 v45, 0xffff0000, v116
	v_lshlrev_b32_e32 v34, 16, v117
	v_and_b32_e32 v35, 0xffff0000, v117
	v_lshlrev_b32_e32 v42, 16, v118
	v_and_b32_e32 v43, 0xffff0000, v118
	v_lshlrev_b32_e32 v36, 16, v119
	v_and_b32_e32 v37, 0xffff0000, v119
	v_lshlrev_b32_e32 v38, 16, v120
	v_and_b32_e32 v39, 0xffff0000, v120
	v_lshlrev_b32_e32 v40, 16, v121
	v_and_b32_e32 v41, 0xffff0000, v121
	s_cbranch_scc1 .LBB0_676
	v_add_co_u32_e32 v48, vcc, 0xff200000, v28
	v_lshl_add_u64 v[56:57], v[28:29], 0, s[14:15]
	s_nop 0
	v_addc_co_u32_e32 v49, vcc, -1, v29, vcc
	v_add_co_u32_e32 v52, vcc, s7, v28
	global_load_dwordx2 v[46:47], v[48:49], off offset:-1536
	s_nop 0
	v_addc_co_u32_e32 v53, vcc, -1, v29, vcc
	v_add_co_u32_e32 v62, vcc, s9, v28
	global_load_dwordx2 v[50:51], v[52:53], off offset:-1536
	s_nop 0
	v_addc_co_u32_e32 v63, vcc, -1, v29, vcc
	v_add_co_u32_e32 v76, vcc, s22, v28
	global_load_dwordx2 v[54:55], v[62:63], off offset:-1536
	s_nop 0
	v_addc_co_u32_e32 v77, vcc, -1, v29, vcc
	v_add_co_u32_e32 v78, vcc, s23, v28
	global_load_dwordx2 v[60:61], v[76:77], off offset:-1536
	s_nop 0
	v_addc_co_u32_e32 v79, vcc, -1, v29, vcc
	v_add_co_u32_e32 v70, vcc, s30, v28
	global_load_dwordx2 v[74:75], v[78:79], off offset:-1536
	s_nop 0
	v_addc_co_u32_e32 v71, vcc, -1, v29, vcc
	global_load_dwordx2 v[72:73], v[70:71], off offset:-1536
	v_add_co_u32_e32 v64, vcc, s31, v28
	s_nop 1
	v_addc_co_u32_e32 v65, vcc, -1, v29, vcc
	global_load_dwordx2 v[68:69], v[64:65], off offset:-1536
	global_load_dwordx2 v[58:59], v[28:29], off offset:-1536
	global_load_dwordx4 v[18:21], v[26:27], off
	global_load_dwordx2 v[66:67], v[48:49], off offset:-1024
	global_load_dwordx2 v[80:81], v[48:49], off offset:-512
	global_load_dwordx2 v[82:83], v[48:49], off
	global_load_dwordx2 v[96:97], v[52:53], off offset:-1024
	global_load_dwordx2 v[98:99], v[52:53], off offset:-512
	global_load_dwordx2 v[84:85], v[52:53], off
	global_load_dwordx2 v[100:101], v[62:63], off offset:-1024
	global_load_dwordx2 v[102:103], v[62:63], off offset:-512
	global_load_dwordx2 v[86:87], v[62:63], off
	global_load_dwordx2 v[104:105], v[76:77], off offset:-1024
	global_load_dwordx2 v[106:107], v[76:77], off offset:-512
	global_load_dwordx2 v[88:89], v[76:77], off
	global_load_dwordx2 v[108:109], v[78:79], off offset:-1024
	global_load_dwordx2 v[110:111], v[78:79], off offset:-512
	global_load_dwordx2 v[90:91], v[78:79], off
	s_waitcnt vmcnt(23)
	v_lshlrev_b32_e32 v48, 16, v46
	v_and_b32_e32 v49, 0xffff0000, v46
	v_lshlrev_b32_e32 v46, 16, v47
	v_and_b32_e32 v47, 0xffff0000, v47
	v_pk_add_f32 v[48:49], v[48:49], 0 op_sel_hi:[1,0]
	v_pk_add_f32 v[46:47], v[46:47], 0 op_sel_hi:[1,0]
	s_waitcnt vmcnt(22)
	v_lshlrev_b32_e32 v52, 16, v50
	v_and_b32_e32 v53, 0xffff0000, v50
	v_lshlrev_b32_e32 v50, 16, v51
	v_and_b32_e32 v51, 0xffff0000, v51
	v_pk_add_f32 v[46:47], v[46:47], v[50:51]
	v_pk_add_f32 v[48:49], v[48:49], v[52:53]
	s_waitcnt vmcnt(21)
	v_lshlrev_b32_e32 v50, 16, v54
	v_and_b32_e32 v51, 0xffff0000, v54
	v_lshlrev_b32_e32 v52, 16, v55
	v_and_b32_e32 v53, 0xffff0000, v55
	v_pk_add_f32 v[48:49], v[48:49], v[50:51]
	v_pk_add_f32 v[46:47], v[46:47], v[52:53]
	s_waitcnt vmcnt(20)
	v_lshlrev_b32_e32 v50, 16, v60
	v_and_b32_e32 v51, 0xffff0000, v60
	v_lshlrev_b32_e32 v52, 16, v61
	v_and_b32_e32 v53, 0xffff0000, v61
	v_pk_add_f32 v[46:47], v[46:47], v[52:53]
	v_pk_add_f32 v[48:49], v[48:49], v[50:51]
	s_waitcnt vmcnt(19)
	v_lshlrev_b32_e32 v50, 16, v74
	v_and_b32_e32 v51, 0xffff0000, v74
	v_lshlrev_b32_e32 v52, 16, v75
	v_and_b32_e32 v53, 0xffff0000, v75
	v_pk_add_f32 v[48:49], v[48:49], v[50:51]
	v_pk_add_f32 v[46:47], v[46:47], v[52:53]
	s_waitcnt vmcnt(18)
	v_lshlrev_b32_e32 v60, 16, v72
	v_and_b32_e32 v61, 0xffff0000, v72
	v_lshlrev_b32_e32 v62, 16, v73
	v_and_b32_e32 v63, 0xffff0000, v73
	global_load_dwordx2 v[50:51], v[70:71], off offset:-1024
	global_load_dwordx2 v[52:53], v[70:71], off offset:-512
	global_load_dwordx2 v[54:55], v[70:71], off
	v_pk_add_f32 v[46:47], v[46:47], v[62:63]
	v_pk_add_f32 v[48:49], v[48:49], v[60:61]
	global_load_dwordx2 v[60:61], v[64:65], off offset:-1024
	global_load_dwordx2 v[62:63], v[64:65], off offset:-512
	global_load_dwordx2 v[70:71], v[64:65], off
	s_waitcnt vmcnt(23)
	v_lshlrev_b32_e32 v64, 16, v68
	v_and_b32_e32 v65, 0xffff0000, v68
	v_lshlrev_b32_e32 v68, 16, v69
	v_and_b32_e32 v69, 0xffff0000, v69
	v_pk_add_f32 v[48:49], v[48:49], v[64:65]
	s_waitcnt vmcnt(22)
	v_lshlrev_b32_e32 v74, 16, v58
	v_and_b32_e32 v75, 0xffff0000, v58
	v_pk_add_f32 v[46:47], v[46:47], v[68:69]
	v_lshlrev_b32_e32 v58, 16, v59
	v_and_b32_e32 v59, 0xffff0000, v59
	v_pk_add_f32 v[48:49], v[48:49], v[74:75]
	v_pk_add_f32 v[46:47], v[46:47], v[58:59]
	s_waitcnt vmcnt(21)
	v_pk_fma_f32 v[18:19], v[48:49], v[18:19], v[30:31]
	v_pk_fma_f32 v[32:33], v[46:47], v[20:21], v[32:33]
	v_bfe_u32 v20, v18, 16, 1
	v_add3_u32 v30, v18, v20, s33
	v_bfe_u32 v18, v19, 16, 1
	v_and_b32_sdwa v20, v33, v95 dst_sel:DWORD dst_unused:UNUSED_PAD src0_sel:WORD_1 src1_sel:DWORD
	v_add3_u32 v18, v19, v18, s33
	v_bfe_u32 v19, v32, 16, 1
	v_add3_u32 v20, v33, v20, s33
	v_and_b32_e32 v31, 0xffff0000, v18
	v_add3_u32 v19, v32, v19, s33
	v_and_b32_e32 v33, 0xffff0000, v20
	v_or_b32_sdwa v18, v31, v30 dst_sel:DWORD dst_unused:UNUSED_PAD src0_sel:DWORD src1_sel:WORD_1
	v_or_b32_sdwa v19, v33, v19 dst_sel:DWORD dst_unused:UNUSED_PAD src0_sel:DWORD src1_sel:WORD_1
	global_load_dwordx2 v[64:65], v[28:29], off offset:-1024
	global_load_dwordx2 v[68:69], v[28:29], off offset:-512
	global_load_dwordx2 v[72:73], v[28:29], off
	s_waitcnt vmcnt(23)
	v_lshlrev_b32_e32 v48, 16, v66
	global_store_dwordx2 v[56:57], v[18:19], off
	global_load_dwordx4 v[18:21], v[26:27], off offset:1024
	v_and_b32_e32 v49, 0xffff0000, v66
	v_lshlrev_b32_e32 v56, 16, v67
	v_and_b32_e32 v57, 0xffff0000, v67
	v_pk_add_f32 v[56:57], v[56:57], 0 op_sel_hi:[1,0]
	v_pk_add_f32 v[48:49], v[48:49], 0 op_sel_hi:[1,0]
	s_waitcnt vmcnt(22)
	v_lshlrev_b32_e32 v58, 16, v96
	v_and_b32_e32 v59, 0xffff0000, v96
	v_lshlrev_b32_e32 v66, 16, v97
	v_and_b32_e32 v67, 0xffff0000, v97
	v_pk_add_f32 v[48:49], v[48:49], v[58:59]
	v_pk_add_f32 v[56:57], v[56:57], v[66:67]
	s_waitcnt vmcnt(19)
	v_lshlrev_b32_e32 v58, 16, v100
	v_and_b32_e32 v59, 0xffff0000, v100
	v_lshlrev_b32_e32 v66, 16, v101
	v_and_b32_e32 v67, 0xffff0000, v101
	v_pk_add_f32 v[56:57], v[56:57], v[66:67]
	v_pk_add_f32 v[48:49], v[48:49], v[58:59]
	s_waitcnt vmcnt(16)
	v_lshlrev_b32_e32 v58, 16, v104
	v_and_b32_e32 v59, 0xffff0000, v104
	v_lshlrev_b32_e32 v66, 16, v105
	v_and_b32_e32 v67, 0xffff0000, v105
	v_pk_add_f32 v[48:49], v[48:49], v[58:59]
	v_pk_add_f32 v[56:57], v[56:57], v[66:67]
	s_waitcnt vmcnt(13)
	v_lshlrev_b32_e32 v58, 16, v108
	v_and_b32_e32 v59, 0xffff0000, v108
	v_lshlrev_b32_e32 v66, 16, v109
	v_and_b32_e32 v67, 0xffff0000, v109
	v_pk_add_f32 v[56:57], v[56:57], v[66:67]
	v_pk_add_f32 v[48:49], v[48:49], v[58:59]
	v_lshl_add_u64 v[46:47], v[28:29], 0, s[16:17]
	v_and_b32_e32 v30, 0xffff0000, v30
	s_waitcnt vmcnt(10)
	v_lshlrev_b32_e32 v58, 16, v50
	v_and_b32_e32 v59, 0xffff0000, v50
	v_lshlrev_b32_e32 v50, 16, v51
	v_and_b32_e32 v51, 0xffff0000, v51
	v_pk_add_f32 v[48:49], v[48:49], v[58:59]
	v_pk_add_f32 v[50:51], v[56:57], v[50:51]
	s_waitcnt vmcnt(7)
	v_lshlrev_b32_e32 v56, 16, v60
	v_and_b32_e32 v57, 0xffff0000, v60
	v_pk_add_f32 v[48:49], v[48:49], v[56:57]
	v_lshlrev_b32_e32 v58, 16, v61
	v_and_b32_e32 v59, 0xffff0000, v61
	v_pk_add_f32 v[50:51], v[50:51], v[58:59]
	v_lshlrev_b32_e32 v60, 16, v98
	v_and_b32_e32 v61, 0xffff0000, v98
	s_waitcnt vmcnt(4)
	v_lshlrev_b32_e32 v56, 16, v64
	v_and_b32_e32 v57, 0xffff0000, v64
	v_pk_add_f32 v[48:49], v[48:49], v[56:57]
	v_lshlrev_b32_e32 v58, 16, v65
	v_and_b32_e32 v59, 0xffff0000, v65
	s_waitcnt vmcnt(0)
	v_pk_fma_f32 v[44:45], v[48:49], v[18:19], v[44:45]
	v_pk_add_f32 v[50:51], v[50:51], v[58:59]
	v_pk_fma_f32 v[34:35], v[50:51], v[20:21], v[34:35]
	v_and_b32_sdwa v20, v35, v95 dst_sel:DWORD dst_unused:UNUSED_PAD src0_sel:WORD_1 src1_sel:DWORD
	v_cvt_pk_bf16_f32 v18, v44, v45
	v_bfe_u32 v19, v34, 16, 1
	v_add3_u32 v20, v35, v20, s33
	v_add3_u32 v19, v34, v19, s33
	v_and_b32_e32 v35, 0xffff0000, v20
	v_or_b32_sdwa v19, v35, v19 dst_sel:DWORD dst_unused:UNUSED_PAD src0_sel:DWORD src1_sel:WORD_1
	global_store_dwordx2 v[46:47], v[18:19], off
	global_load_dwordx4 v[18:21], v[26:27], off offset:2048
	v_lshlrev_b32_e32 v56, 16, v80
	v_and_b32_e32 v57, 0xffff0000, v80
	v_lshlrev_b32_e32 v58, 16, v81
	v_and_b32_e32 v59, 0xffff0000, v81
	v_pk_add_f32 v[58:59], v[58:59], 0 op_sel_hi:[1,0]
	v_pk_add_f32 v[56:57], v[56:57], 0 op_sel_hi:[1,0]
	v_lshlrev_b32_e32 v64, 16, v99
	v_and_b32_e32 v65, 0xffff0000, v99
	v_pk_add_f32 v[56:57], v[56:57], v[60:61]
	v_pk_add_f32 v[58:59], v[58:59], v[64:65]
	v_lshlrev_b32_e32 v60, 16, v102
	v_and_b32_e32 v61, 0xffff0000, v102
	v_lshlrev_b32_e32 v64, 16, v103
	v_and_b32_e32 v65, 0xffff0000, v103
	v_pk_add_f32 v[58:59], v[58:59], v[64:65]
	v_pk_add_f32 v[56:57], v[56:57], v[60:61]
	v_lshlrev_b32_e32 v60, 16, v106
	v_and_b32_e32 v61, 0xffff0000, v106
	v_lshlrev_b32_e32 v64, 16, v107
	v_and_b32_e32 v65, 0xffff0000, v107
	v_pk_add_f32 v[56:57], v[56:57], v[60:61]
	v_pk_add_f32 v[58:59], v[58:59], v[64:65]
	v_lshlrev_b32_e32 v60, 16, v110
	v_and_b32_e32 v61, 0xffff0000, v110
	v_lshlrev_b32_e32 v64, 16, v111
	v_and_b32_e32 v65, 0xffff0000, v111
	v_pk_add_f32 v[58:59], v[58:59], v[64:65]
	v_pk_add_f32 v[56:57], v[56:57], v[60:61]
	v_lshlrev_b32_e32 v60, 16, v52
	v_and_b32_e32 v61, 0xffff0000, v52
	v_lshlrev_b32_e32 v52, 16, v53
	v_and_b32_e32 v53, 0xffff0000, v53
	v_pk_add_f32 v[56:57], v[56:57], v[60:61]
	v_pk_add_f32 v[52:53], v[58:59], v[52:53]
	v_lshlrev_b32_e32 v58, 16, v62
	v_and_b32_e32 v59, 0xffff0000, v62
	v_lshlrev_b32_e32 v60, 16, v63
	v_and_b32_e32 v61, 0xffff0000, v63
	v_lshlrev_b32_e32 v48, 16, v68
	v_and_b32_e32 v49, 0xffff0000, v68
	v_lshlrev_b32_e32 v50, 16, v69
	v_and_b32_e32 v51, 0xffff0000, v69
	v_pk_add_f32 v[52:53], v[52:53], v[60:61]
	v_pk_add_f32 v[56:57], v[56:57], v[58:59]
	v_pk_add_f32 v[50:51], v[52:53], v[50:51]
	v_pk_add_f32 v[48:49], v[56:57], v[48:49]
	v_lshl_add_u64 v[46:47], v[28:29], 0, s[18:19]
	v_lshlrev_b32_e32 v52, 16, v82
	v_and_b32_e32 v53, 0xffff0000, v82
	v_lshlrev_b32_e32 v56, 16, v83
	v_and_b32_e32 v57, 0xffff0000, v83
	v_pk_add_f32 v[56:57], v[56:57], 0 op_sel_hi:[1,0]
	v_pk_add_f32 v[52:53], v[52:53], 0 op_sel_hi:[1,0]
	v_lshlrev_b32_e32 v58, 16, v84
	v_and_b32_e32 v59, 0xffff0000, v84
	v_lshlrev_b32_e32 v60, 16, v85
	v_and_b32_e32 v61, 0xffff0000, v85
	v_pk_add_f32 v[52:53], v[52:53], v[58:59]
	v_pk_add_f32 v[56:57], v[56:57], v[60:61]
	v_lshlrev_b32_e32 v58, 16, v86
	v_and_b32_e32 v59, 0xffff0000, v86
	v_lshlrev_b32_e32 v60, 16, v87
	v_and_b32_e32 v61, 0xffff0000, v87
	v_pk_add_f32 v[56:57], v[56:57], v[60:61]
	v_pk_add_f32 v[52:53], v[52:53], v[58:59]
	v_lshlrev_b32_e32 v58, 16, v88
	v_and_b32_e32 v59, 0xffff0000, v88
	v_lshlrev_b32_e32 v60, 16, v89
	v_and_b32_e32 v61, 0xffff0000, v89
	v_pk_add_f32 v[52:53], v[52:53], v[58:59]
	v_pk_add_f32 v[56:57], v[56:57], v[60:61]
	v_lshlrev_b32_e32 v58, 16, v90
	v_and_b32_e32 v59, 0xffff0000, v90
	v_lshlrev_b32_e32 v60, 16, v91
	v_and_b32_e32 v61, 0xffff0000, v91
	v_pk_add_f32 v[56:57], v[56:57], v[60:61]
	v_pk_add_f32 v[52:53], v[52:53], v[58:59]
	v_lshlrev_b32_e32 v58, 16, v54
	v_and_b32_e32 v59, 0xffff0000, v54
	s_waitcnt vmcnt(0)
	v_pk_fma_f32 v[36:37], v[50:51], v[20:21], v[36:37]
	v_pk_fma_f32 v[42:43], v[48:49], v[18:19], v[42:43]
	v_and_b32_sdwa v21, v37, v95 dst_sel:DWORD dst_unused:UNUSED_PAD src0_sel:WORD_1 src1_sel:DWORD
	v_bfe_u32 v20, v36, 16, 1
	v_add3_u32 v21, v37, v21, s33
	v_add3_u32 v20, v36, v20, s33
	v_and_b32_e32 v37, 0xffff0000, v21
	v_cvt_pk_bf16_f32 v18, v42, v43
	v_or_b32_sdwa v19, v37, v20 dst_sel:DWORD dst_unused:UNUSED_PAD src0_sel:DWORD src1_sel:WORD_1
	global_store_dwordx2 v[46:47], v[18:19], off
	global_load_dwordx4 v[18:21], v[26:27], off offset:3072
	v_lshlrev_b32_e32 v54, 16, v55
	v_and_b32_e32 v55, 0xffff0000, v55
	v_pk_add_f32 v[52:53], v[52:53], v[58:59]
	v_pk_add_f32 v[54:55], v[56:57], v[54:55]
	v_lshlrev_b32_e32 v56, 16, v70
	v_and_b32_e32 v57, 0xffff0000, v70
	v_lshlrev_b32_e32 v58, 16, v71
	v_and_b32_e32 v59, 0xffff0000, v71
	v_lshlrev_b32_e32 v48, 16, v72
	v_and_b32_e32 v49, 0xffff0000, v72
	v_lshlrev_b32_e32 v50, 16, v73
	v_and_b32_e32 v51, 0xffff0000, v73
	v_pk_add_f32 v[54:55], v[54:55], v[58:59]
	v_pk_add_f32 v[52:53], v[52:53], v[56:57]
	v_pk_add_f32 v[50:51], v[54:55], v[50:51]
	v_pk_add_f32 v[48:49], v[52:53], v[48:49]
	v_and_b32_sdwa v52, v32, v95 dst_sel:DWORD dst_unused:UNUSED_PAD src0_sel:WORD_1 src1_sel:DWORD
	v_add3_u32 v32, v32, v52, s33
	v_and_b32_sdwa v52, v45, v95 dst_sel:DWORD dst_unused:UNUSED_PAD src0_sel:WORD_1 src1_sel:DWORD
	v_and_b32_sdwa v53, v44, v95 dst_sel:DWORD dst_unused:UNUSED_PAD src0_sel:WORD_1 src1_sel:DWORD
	v_and_b32_sdwa v54, v34, v95 dst_sel:DWORD dst_unused:UNUSED_PAD src0_sel:WORD_1 src1_sel:DWORD
	v_add3_u32 v45, v45, v52, s33
	v_add3_u32 v44, v44, v53, s33
	v_add3_u32 v34, v34, v54, s33
	v_and_b32_sdwa v52, v43, v95 dst_sel:DWORD dst_unused:UNUSED_PAD src0_sel:WORD_1 src1_sel:DWORD
	v_and_b32_sdwa v53, v42, v95 dst_sel:DWORD dst_unused:UNUSED_PAD src0_sel:WORD_1 src1_sel:DWORD
	v_and_b32_sdwa v54, v36, v95 dst_sel:DWORD dst_unused:UNUSED_PAD src0_sel:WORD_1 src1_sel:DWORD
	v_add3_u32 v43, v43, v52, s33
	v_add3_u32 v42, v42, v53, s33
	v_add3_u32 v36, v36, v54, s33
	v_lshl_add_u64 v[46:47], v[28:29], 0, s[20:21]
	v_and_b32_e32 v32, 0xffff0000, v32
	v_and_b32_e32 v45, 0xffff0000, v45
	v_and_b32_e32 v44, 0xffff0000, v44
	v_and_b32_e32 v34, 0xffff0000, v34
	v_and_b32_e32 v43, 0xffff0000, v43
	v_and_b32_e32 v42, 0xffff0000, v42
	v_and_b32_e32 v36, 0xffff0000, v36
	s_waitcnt vmcnt(0)
	v_pk_fma_f32 v[20:21], v[50:51], v[20:21], v[40:41]
	v_pk_fma_f32 v[18:19], v[48:49], v[18:19], v[38:39]
	v_and_b32_sdwa v49, v21, v95 dst_sel:DWORD dst_unused:UNUSED_PAD src0_sel:WORD_1 src1_sel:DWORD
	v_bfe_u32 v38, v18, 16, 1
	v_bfe_u32 v39, v19, 16, 1
	v_bfe_u32 v40, v20, 16, 1
	v_and_b32_sdwa v41, v19, v95 dst_sel:DWORD dst_unused:UNUSED_PAD src0_sel:WORD_1 src1_sel:DWORD
	v_and_b32_sdwa v48, v18, v95 dst_sel:DWORD dst_unused:UNUSED_PAD src0_sel:WORD_1 src1_sel:DWORD
	v_and_b32_sdwa v50, v20, v95 dst_sel:DWORD dst_unused:UNUSED_PAD src0_sel:WORD_1 src1_sel:DWORD
	v_add3_u32 v38, v18, v38, s33
	v_add3_u32 v21, v21, v49, s33
	v_add3_u32 v51, v19, v39, s33
	v_add3_u32 v52, v20, v40, s33
	v_add3_u32 v19, v19, v41, s33
	v_add3_u32 v18, v18, v48, s33
	v_add3_u32 v20, v20, v50, s33
	v_lshrrev_b32_e32 v40, 16, v38
	v_and_b32_e32 v41, 0xffff0000, v21
	v_and_b32_e32 v39, 0xffff0000, v19
	v_and_b32_e32 v38, 0xffff0000, v18
	v_and_or_b32 v18, v51, s3, v40
	v_and_b32_e32 v40, 0xffff0000, v20
	v_or_b32_sdwa v19, v41, v52 dst_sel:DWORD dst_unused:UNUSED_PAD src0_sel:DWORD src1_sel:WORD_1
	global_store_dwordx2 v[46:47], v[18:19], off
	s_branch .LBB0_676

.LBB0_888:
	s_cmp_lt_i32 s92, 11
	s_cselect_b64 s[4:5], -1, 0
	s_cmp_gt_i32 s93, 10
	s_cselect_b64 s[6:7], -1, 0
	s_and_b64 s[4:5], s[4:5], s[6:7]
	s_andn2_b64 vcc, exec, s[4:5]
	s_cbranch_vccnz .LBB0_944
	s_lshl_b32 s3, s89, 3
	s_add_i32 s6, s3, s88
	s_cmpk_gt_i32 s6, 0x43ff
	s_mov_b32 s4, 6
	s_cbranch_scc1 .LBB0_894
	s_ashr_i32 s5, s4, 31
	s_lshl_b32 s8, s34, 3
	s_lshl_b64 s[4:5], s[4:5], 3
	s_add_u32 s4, s0, s4
	s_addc_u32 s5, s1, s5
	s_load_dwordx2 s[4:5], s[4:5], 0x0
	s_waitcnt vmcnt(0)
	v_lshlrev_b32_e32 v18, 2, v250
	v_ashrrev_i32_e32 v19, 31, v18
	v_lshlrev_b64 v[20:21], 2, v[18:19]
	v_mbcnt_lo_u32_b32 v1, -1, 0
	s_waitcnt lgkmcnt(0)
	v_lshl_add_u64 v[2:3], s[4:5], 0, v[20:21]
	s_mov_b64 s[4:5], 0x1000
	v_lshl_add_u64 v[22:23], v[2:3], 0, s[4:5]
	v_add_co_u32_e32 v24, vcc, 0x1000, v2
	v_lshl_add_u64 v[20:21], s[26:27], 0, v[20:21]
	s_nop 0
	v_addc_co_u32_e32 v25, vcc, 0, v3, vcc
	global_load_dwordx4 v[2:5], v[22:23], off offset:1024
	global_load_dwordx4 v[6:9], v[22:23], off offset:2048
	global_load_dwordx4 v[10:13], v[24:25], off
	global_load_dwordx4 v[14:17], v[22:23], off offset:3072
	v_mbcnt_hi_u32_b32 v22, -1, v1
	v_and_b32_e32 v23, 64, v22
	v_xor_b32_e32 v1, 16, v22
	v_add_u32_e32 v23, 64, v23
	v_cmp_lt_i32_e32 vcc, v1, v23
	v_xor_b32_e32 v24, 32, v22
	s_mov_b64 s[4:5], 0x11e000
	v_cndmask_b32_e32 v1, v22, v1, vcc
	v_cmp_lt_i32_e32 vcc, v24, v23
	s_ashr_i32 s7, s6, 31
	s_mov_b32 s14, 0xdcbffa00
	v_cndmask_b32_e32 v22, v22, v24, vcc
	v_lshlrev_b32_e32 v94, 2, v22
	v_lshl_add_u64 v[22:23], v[20:21], 0, s[4:5]
	s_mov_b64 s[4:5], 0x11f000
	v_lshl_add_u64 v[24:25], v[20:21], 0, s[4:5]
	s_mov_b64 s[4:5], 0x11d000
	v_lshl_add_u64 v[26:27], v[20:21], 0, s[4:5]
	s_lshl_b64 s[4:5], s[6:7], 11
	s_add_u32 s4, s26, s4
	s_addc_u32 s5, s27, s5
	v_lshl_add_u64 v[18:19], v[18:19], 1, s[4:5]
	s_mov_b64 s[4:5], 0x3eb00600
	s_ashr_i32 s9, s8, 31
	s_mov_b32 s16, 0xdcbffc00
	s_mov_b32 s18, 0xdcbffe00
	s_mov_b32 s20, 0xdcc00000
	s_mov_b32 s11, 0
	v_lshlrev_b32_e32 v1, 2, v1
	v_lshl_add_u64 v[28:29], v[18:19], 0, s[4:5]
	s_lshl_b64 s[12:13], s[8:9], 11
	s_mov_b32 s15, -1
	s_mov_b32 s3, 0xffff0000
	s_mov_b32 s17, -1
	s_mov_b32 s19, -1
	s_mov_b32 s21, -1
	s_mov_b32 s7, 0xfee00000
	s_mov_b32 s9, 0xff000000
	s_mov_b32 s22, 0xff200000
	s_mov_b32 s23, 0xff400000
	s_mov_b32 s30, 0xff600000
	s_mov_b32 s31, 0xff800000
	s_mov_b32 s33, 0xffa00000
	s_mov_b32 s35, 0xffc00000
	s_mov_b32 s36, 0xffe00000
	s_movk_i32 s37, 0x7fff
	v_mov_b32_e32 v95, 0x358637bd
	s_mov_b32 s42, 0xf800000
	v_mov_b32_e32 v96, 0x260
	s_mov_b32 s43, 0xe1000000
	v_mov_b32_e32 v97, 1
	v_add_co_u32_e32 v126, vcc, 0xdcc00000, v28
	s_nop 1
	v_addc_co_u32_e32 v127, vcc, -1, v29, vcc
	global_load_dwordx2 v[128:129], v[126:127], off offset:-1536
	global_load_dwordx2 v[132:133], v[126:127], off offset:-1024
	global_load_dwordx2 v[136:137], v[126:127], off offset:-512
	global_load_dwordx2 v[138:139], v[126:127], off
	s_waitcnt vmcnt(0)
	s_branch .LBB0_892
.LBB0_891:
	v_pk_mul_f32 v[62:63], v[32:33], v[32:33]
	v_pk_mul_f32 v[64:65], v[30:31], v[30:31]
	v_pk_mul_f32 v[58:59], v[34:35], v[34:35]
	v_pk_mul_f32 v[60:61], v[38:39], v[38:39]
	v_pk_mov_b32 v[66:67], v[64:65], v[62:63] op_sel:[1,0]
	v_mov_b32_e32 v65, v63
	v_pk_add_f32 v[62:63], v[66:67], v[64:65]
	v_pk_mov_b32 v[64:65], v[60:61], v[58:59] op_sel:[1,0]
	v_mov_b32_e32 v61, v59
	v_pk_add_f32 v[58:59], v[64:65], v[60:61]
	s_add_i32 s10, s6, 0xfffffc00
	v_pk_add_f32 v[58:59], v[58:59], v[58:59] op_sel_hi:[0,1]
	v_mul_f32_e32 v58, v44, v44
	s_lshr_b32 s10, s10, 12
	v_pk_fma_f32 v[60:61], v[44:45], v[44:45], v[58:59] op_sel_hi:[1,1,0]
	v_mul_f32_e32 v58, v40, v40
	s_mulk_i32 s10, 0x1800
	s_and_b64 s[4:5], s[4:5], exec
	v_pk_add_f32 v[62:63], v[62:63], v[62:63] op_sel_hi:[0,1]
	v_pk_fma_f32 v[64:65], v[40:41], v[40:41], v[58:59] op_sel_hi:[1,1,0]
	s_cselect_b32 s10, 0x6000, s10
	v_mul_f32_e32 v60, v36, v36
	v_mul_f32_e32 v64, v37, v37
	v_mul_f32_e32 v62, v42, v42
	v_mul_f32_e32 v58, v43, v43
	s_lshl_b64 s[4:5], s[10:11], 2
	v_pk_add_f32 v[66:67], v[60:61], v[64:65]
	v_pk_add_f32 v[68:69], v[62:63], v[58:59]
	v_lshl_add_u64 v[54:55], v[24:25], 0, s[4:5]
	v_lshl_add_u64 v[70:71], v[22:23], 0, s[4:5]
	v_pk_add_f32 v[66:67], v[66:67], v[68:69]
	global_load_dwordx4 v[18:21], v[54:55], off
	global_load_dwordx4 v[46:49], v[54:55], off offset:1024
	global_load_dwordx4 v[50:53], v[54:55], off offset:2048
	s_nop 0
	global_load_dwordx4 v[54:57], v[54:55], off offset:3072
	s_nop 0
	global_load_dwordx4 v[58:61], v[70:71], off offset:2048
	global_load_dwordx4 v[62:65], v[70:71], off offset:3072
	v_add_f32_e32 v74, v66, v67
	global_load_dwordx4 v[66:69], v[70:71], off
	s_nop 0
	global_load_dwordx4 v[70:73], v[70:71], off offset:1024
	v_lshl_add_u64 v[126:127], v[126:127], 0, s[12:13]
	global_load_dwordx2 v[128:129], v[126:127], off offset:-1536
	global_load_dwordx2 v[132:133], v[126:127], off offset:-1024
	global_load_dwordx2 v[136:137], v[126:127], off offset:-512
	global_load_dwordx2 v[138:139], v[126:127], off
	v_add_f32_dpp v74, v74, v74 row_ror:8 row_mask:0xf bank_mask:0xf bound_ctrl:1
	s_add_i32 s6, s6, s8
	s_cmpk_lt_i32 s6, 0x4400
	v_add_f32_dpp v74, v74, v74 row_ror:4 row_mask:0xf bank_mask:0xf bound_ctrl:1
	s_waitcnt vmcnt(11)
	v_pk_add_f32 v[18:19], v[18:19], 1.0 op_sel_hi:[1,0]
	v_add_f32_dpp v74, v74, v74 row_ror:2 row_mask:0xf bank_mask:0xf bound_ctrl:1
	v_pk_add_f32 v[20:21], v[20:21], 1.0 op_sel_hi:[1,0]
	s_waitcnt vmcnt(10)
	v_pk_add_f32 v[46:47], v[46:47], 1.0 op_sel_hi:[1,0]
	v_add_f32_dpp v74, v74, v74 row_ror:1 row_mask:0xf bank_mask:0xf bound_ctrl:1
	v_mov_b32_e32 v75, v74
	s_nop 1
	v_permlane16_swap_b32_e32 v74, v75
	v_pk_add_f32 v[48:49], v[48:49], 1.0 op_sel_hi:[1,0]
	s_waitcnt vmcnt(9)
	v_pk_add_f32 v[50:51], v[50:51], 1.0 op_sel_hi:[1,0]
	v_pk_add_f32 v[52:53], v[52:53], 1.0 op_sel_hi:[1,0]
	s_waitcnt vmcnt(8)
	v_pk_add_f32 v[54:55], v[54:55], 1.0 op_sel_hi:[1,0]
	s_waitcnt lgkmcnt(0)
	v_add_f32_e32 v74, v74, v75
	v_mov_b32_e32 v75, v74
	s_nop 1
	v_permlane32_swap_b32_e32 v74, v75
	v_pk_add_f32 v[56:57], v[56:57], 1.0 op_sel_hi:[1,0]
	s_waitcnt lgkmcnt(0)
	v_add_f32_e32 v74, v74, v75
	v_fmamk_f32 v74, v74, 0x3a800000, v95
	v_mul_f32_e32 v75, 0x4f800000, v74
	v_cmp_gt_f32_e32 vcc, s42, v74
	s_nop 1
	v_cndmask_b32_e32 v74, v74, v75, vcc
	v_sqrt_f32_e32 v75, v74
	s_nop 0
	v_add_u32_e32 v76, -1, v75
	v_add_u32_e32 v77, 1, v75
	v_fma_f32 v78, -v76, v75, v74
	v_fma_f32 v79, -v77, v75, v74
	v_cmp_ge_f32_e64 s[4:5], 0, v78
	s_nop 1
	v_cndmask_b32_e64 v75, v75, v76, s[4:5]
	v_cmp_lt_f32_e64 s[4:5], 0, v79
	s_nop 1
	v_cndmask_b32_e64 v75, v75, v77, s[4:5]
	v_mul_f32_e32 v76, 0x37800000, v75
	v_cndmask_b32_e32 v75, v75, v76, vcc
	v_cmp_class_f32_e32 vcc, v74, v96
	s_nop 1
	v_cndmask_b32_e32 v74, v75, v74, vcc
	v_div_scale_f32 v75, s[4:5], v74, v74, 1.0
	v_rcp_f32_e32 v76, v75
	v_div_scale_f32 v77, vcc, 1.0, v74, 1.0
	v_fma_f32 v78, -v75, v76, 1.0
	v_fmac_f32_e32 v76, v78, v76
	v_mul_f32_e32 v78, v77, v76
	v_fma_f32 v79, -v75, v78, v77
	v_fmac_f32_e32 v78, v79, v76
	v_fma_f32 v75, -v75, v78, v77
	v_div_fmas_f32 v75, v75, v76, v78
	v_div_fixup_f32 v74, v75, v74, 1.0
	v_pk_mul_f32 v[30:31], v[30:31], v[74:75] op_sel_hi:[1,0]
	v_pk_mul_f32 v[32:33], v[32:33], v[74:75] op_sel_hi:[1,0]
	v_pk_mul_f32 v[30:31], v[10:11], v[30:31]
	v_pk_mul_f32 v[32:33], v[12:13], v[32:33]
	s_waitcnt vmcnt(5)
	v_pk_fma_f32 v[18:19], v[18:19], v[30:31], v[66:67]
	v_pk_fma_f32 v[20:21], v[20:21], v[32:33], v[68:69]
	v_bfe_u32 v30, v18, 16, 1
	v_add3_u32 v18, v18, v30, s37
	v_bfe_u32 v30, v19, 16, 1
	v_lshrrev_b32_e32 v18, 16, v18
	v_add3_u32 v19, v19, v30, s37
	v_and_or_b32 v18, v19, s3, v18
	v_bfe_u32 v19, v20, 16, 1
	v_add3_u32 v19, v20, v19, s37
	v_bfe_u32 v20, v21, 16, 1
	v_pk_mul_f32 v[38:39], v[38:39], v[74:75] op_sel_hi:[1,0]
	v_lshrrev_b32_e32 v19, 16, v19
	v_add3_u32 v20, v21, v20, s37
	v_pk_mul_f32 v[38:39], v[2:3], v[38:39]
	v_and_or_b32 v19, v20, s3, v19
	v_add_co_u32_e32 v20, vcc, s43, v28
	s_waitcnt vmcnt(4)
	v_pk_fma_f32 v[38:39], v[46:47], v[38:39], v[70:71]
	v_addc_co_u32_e32 v21, vcc, -1, v29, vcc
	v_pk_mul_f32 v[34:35], v[34:35], v[74:75] op_sel_hi:[1,0]
	global_store_dwordx2 v[20:21], v[18:19], off offset:-1536
	v_pk_mul_f32 v[34:35], v[4:5], v[34:35]
	v_pk_fma_f32 v[34:35], v[48:49], v[34:35], v[72:73]
	v_cvt_pk_bf16_f32 v18, v38, v39
	v_pk_mul_f32 v[44:45], v[44:45], v[74:75] op_sel_hi:[1,0]
	v_pk_mul_f32 v[44:45], v[6:7], v[44:45]
	v_pk_fma_f32 v[44:45], v[50:51], v[44:45], v[58:59]
	v_cvt_pk_bf16_f32 v19, v34, v35
	v_pk_mul_f32 v[40:41], v[40:41], v[74:75] op_sel_hi:[1,0]
	global_store_dwordx2 v[20:21], v[18:19], off offset:-1024
	v_pk_mul_f32 v[40:41], v[8:9], v[40:41]
	v_pk_fma_f32 v[40:41], v[52:53], v[40:41], v[60:61]
	v_cvt_pk_bf16_f32 v18, v44, v45
	v_pk_mul_f32 v[36:37], v[36:37], v[74:75] op_sel_hi:[1,0]
	v_pk_mul_f32 v[36:37], v[14:15], v[36:37]
	v_pk_fma_f32 v[36:37], v[54:55], v[36:37], v[62:63]
	v_cvt_pk_bf16_f32 v19, v40, v41
	v_pk_mul_f32 v[42:43], v[42:43], v[74:75] op_sel_hi:[1,0]
	global_store_dwordx2 v[20:21], v[18:19], off offset:-512
	v_pk_mul_f32 v[42:43], v[16:17], v[42:43]
	v_pk_fma_f32 v[42:43], v[56:57], v[42:43], v[64:65]
	v_cvt_pk_bf16_f32 v18, v36, v37
	v_cvt_pk_bf16_f32 v19, v42, v43
	v_lshl_add_u64 v[28:29], v[28:29], 0, s[12:13]
	global_store_dwordx2 v[20:21], v[18:19], off
	s_cbranch_scc0 .LBB0_894
.LBB0_892:
	s_waitcnt vmcnt(4)
	s_cmpk_lt_i32 s6, 0x400
	s_cselect_b64 s[4:5], -1, 0
	s_cmpk_gt_i32 s6, 0x3ff
	v_lshlrev_b32_e32 v30, 16, v128
	v_and_b32_e32 v31, 0xffff0000, v128
	v_lshlrev_b32_e32 v32, 16, v129
	v_and_b32_e32 v33, 0xffff0000, v129
	v_lshlrev_b32_e32 v38, 16, v132
	v_and_b32_e32 v39, 0xffff0000, v132
	v_lshlrev_b32_e32 v34, 16, v133
	v_and_b32_e32 v35, 0xffff0000, v133
	v_lshlrev_b32_e32 v44, 16, v136
	v_and_b32_e32 v45, 0xffff0000, v136
	v_lshlrev_b32_e32 v40, 16, v137
	v_and_b32_e32 v41, 0xffff0000, v137
	v_lshlrev_b32_e32 v36, 16, v138
	v_and_b32_e32 v37, 0xffff0000, v138
	v_lshlrev_b32_e32 v42, 16, v139
	v_and_b32_e32 v43, 0xffff0000, v139
	s_cbranch_scc1 .LBB0_891
	v_add_co_u32_e32 v76, vcc, 0xfec00000, v28
	v_lshl_add_u64 v[46:47], v[28:29], 0, s[14:15]
	s_nop 0
	v_addc_co_u32_e32 v77, vcc, -1, v29, vcc
	v_add_co_u32_e32 v74, vcc, s7, v28
	global_load_dwordx2 v[50:51], v[76:77], off offset:-1536
	s_nop 0
	v_addc_co_u32_e32 v75, vcc, -1, v29, vcc
	v_add_co_u32_e32 v78, vcc, s9, v28
	global_load_dwordx2 v[48:49], v[28:29], off offset:-1536
	s_nop 0
	v_addc_co_u32_e32 v79, vcc, -1, v29, vcc
	v_add_co_u32_e32 v66, vcc, s22, v28
	global_load_dwordx2 v[72:73], v[78:79], off offset:-1536
	global_load_dwordx2 v[52:53], v[74:75], off offset:-1536
	v_addc_co_u32_e32 v67, vcc, -1, v29, vcc
	v_add_co_u32_e32 v62, vcc, s23, v28
	global_load_dwordx2 v[70:71], v[66:67], off offset:-1536
	s_nop 0
	v_addc_co_u32_e32 v63, vcc, -1, v29, vcc
	v_add_co_u32_e32 v56, vcc, s30, v28
	global_load_dwordx2 v[68:69], v[62:63], off offset:-1536
	s_nop 0
	v_addc_co_u32_e32 v57, vcc, -1, v29, vcc
	v_add_co_u32_e32 v54, vcc, s31, v28
	global_load_dwordx2 v[64:65], v[56:57], off offset:-1536
	s_nop 0
	v_addc_co_u32_e32 v55, vcc, -1, v29, vcc
	global_load_dwordx2 v[58:59], v[54:55], off offset:-1536
	v_add_co_u32_e32 v84, vcc, s33, v28
	s_waitcnt vmcnt(7)
	v_lshlrev_b32_e32 v106, 16, v50
	v_addc_co_u32_e32 v85, vcc, -1, v29, vcc
	global_load_dwordx2 v[86:87], v[84:85], off offset:-1536
	global_load_dwordx4 v[18:21], v[26:27], off
	v_add_co_u32_e32 v80, vcc, s35, v28
	v_and_b32_e32 v107, 0xffff0000, v50
	s_nop 0
	v_addc_co_u32_e32 v81, vcc, -1, v29, vcc
	global_load_dwordx2 v[82:83], v[80:81], off offset:-1536
	global_load_dwordx2 v[60:61], v[76:77], off offset:-1024
	global_load_dwordx2 v[88:89], v[76:77], off offset:-512
	s_nop 0
	global_load_dwordx2 v[76:77], v[76:77], off
	v_add_co_u32_e32 v98, vcc, s36, v28
	v_lshlrev_b32_e32 v50, 16, v51
	s_nop 0
	v_addc_co_u32_e32 v99, vcc, -1, v29, vcc
	global_load_dwordx2 v[100:101], v[98:99], off offset:-1536
	global_load_dwordx2 v[102:103], v[74:75], off offset:-1024
	global_load_dwordx2 v[90:91], v[74:75], off offset:-512
	s_nop 0
	global_load_dwordx2 v[74:75], v[74:75], off
	s_nop 0
	global_load_dwordx2 v[104:105], v[78:79], off offset:-1024
	global_load_dwordx2 v[92:93], v[78:79], off offset:-512
	s_nop 0
	global_load_dwordx2 v[78:79], v[78:79], off
	v_and_b32_e32 v51, 0xffff0000, v51
	v_pk_add_f32 v[50:51], v[50:51], 0 op_sel_hi:[1,0]
	v_pk_add_f32 v[106:107], v[106:107], 0 op_sel_hi:[1,0]
	s_waitcnt vmcnt(17)
	v_lshlrev_b32_e32 v108, 16, v52
	v_and_b32_e32 v109, 0xffff0000, v52
	v_lshlrev_b32_e32 v52, 16, v53
	v_and_b32_e32 v53, 0xffff0000, v53
	v_pk_add_f32 v[106:107], v[106:107], v[108:109]
	v_pk_add_f32 v[50:51], v[50:51], v[52:53]
	v_lshlrev_b32_e32 v52, 16, v72
	v_and_b32_e32 v53, 0xffff0000, v72
	v_lshlrev_b32_e32 v72, 16, v73
	v_and_b32_e32 v73, 0xffff0000, v73
	v_pk_add_f32 v[108:109], v[50:51], v[72:73]
	v_pk_add_f32 v[52:53], v[106:107], v[52:53]
	global_load_dwordx2 v[106:107], v[66:67], off offset:-1024
	global_load_dwordx2 v[72:73], v[66:67], off offset:-512
	global_load_dwordx2 v[50:51], v[66:67], off
	s_waitcnt vmcnt(19)
	v_lshlrev_b32_e32 v66, 16, v70
	v_and_b32_e32 v67, 0xffff0000, v70
	v_lshlrev_b32_e32 v70, 16, v71
	v_and_b32_e32 v71, 0xffff0000, v71
	v_pk_add_f32 v[66:67], v[52:53], v[66:67]
	v_pk_add_f32 v[108:109], v[108:109], v[70:71]
	global_load_dwordx2 v[110:111], v[62:63], off offset:-1024
	global_load_dwordx2 v[70:71], v[62:63], off offset:-512
	global_load_dwordx2 v[52:53], v[62:63], off
	s_waitcnt vmcnt(21)
	v_lshlrev_b32_e32 v62, 16, v68
	v_and_b32_e32 v63, 0xffff0000, v68
	v_lshlrev_b32_e32 v68, 16, v69
	v_and_b32_e32 v69, 0xffff0000, v69
	v_pk_add_f32 v[108:109], v[108:109], v[68:69]
	v_pk_add_f32 v[62:63], v[66:67], v[62:63]
	s_waitcnt vmcnt(20)
	v_lshlrev_b32_e32 v66, 16, v64
	v_and_b32_e32 v67, 0xffff0000, v64
	v_lshlrev_b32_e32 v64, 16, v65
	v_and_b32_e32 v65, 0xffff0000, v65
	v_pk_add_f32 v[62:63], v[62:63], v[66:67]
	v_pk_add_f32 v[64:65], v[108:109], v[64:65]
	s_waitcnt vmcnt(19)
	v_lshlrev_b32_e32 v66, 16, v58
	v_and_b32_e32 v67, 0xffff0000, v58
	v_lshlrev_b32_e32 v58, 16, v59
	v_and_b32_e32 v59, 0xffff0000, v59
	global_load_dwordx2 v[112:113], v[56:57], off offset:-1024
	global_load_dwordx2 v[68:69], v[56:57], off offset:-512
	s_nop 0
	global_load_dwordx2 v[56:57], v[56:57], off
	s_nop 0
	global_load_dwordx2 v[108:109], v[54:55], off offset:-1024
	global_load_dwordx2 v[114:115], v[54:55], off offset:-512
	s_nop 0
	global_load_dwordx2 v[54:55], v[54:55], off
	v_pk_add_f32 v[64:65], v[64:65], v[58:59]
	v_pk_add_f32 v[62:63], v[62:63], v[66:67]
	global_load_dwordx2 v[116:117], v[84:85], off offset:-1024
	global_load_dwordx2 v[118:119], v[84:85], off offset:-512
	global_load_dwordx2 v[58:59], v[84:85], off
	v_lshlrev_b32_e32 v124, 16, v48
	v_and_b32_e32 v125, 0xffff0000, v48
	v_lshlrev_b32_e32 v48, 16, v49
	v_and_b32_e32 v49, 0xffff0000, v49
	s_waitcnt vmcnt(27)
	v_lshlrev_b32_e32 v66, 16, v86
	v_and_b32_e32 v67, 0xffff0000, v86
	v_lshlrev_b32_e32 v84, 16, v87
	v_and_b32_e32 v85, 0xffff0000, v87
	v_pk_add_f32 v[66:67], v[62:63], v[66:67]
	v_pk_add_f32 v[64:65], v[64:65], v[84:85]
	global_load_dwordx2 v[84:85], v[80:81], off offset:-1024
	global_load_dwordx2 v[86:87], v[80:81], off offset:-512
	global_load_dwordx2 v[62:63], v[80:81], off
	s_waitcnt vmcnt(28)
	v_lshlrev_b32_e32 v80, 16, v82
	v_and_b32_e32 v81, 0xffff0000, v82
	v_lshlrev_b32_e32 v82, 16, v83
	v_and_b32_e32 v83, 0xffff0000, v83
	v_pk_add_f32 v[82:83], v[64:65], v[82:83]
	v_pk_add_f32 v[66:67], v[66:67], v[80:81]
	global_load_dwordx2 v[80:81], v[98:99], off offset:-1024
	global_load_dwordx2 v[120:121], v[98:99], off offset:-512
	global_load_dwordx2 v[64:65], v[98:99], off
	s_waitcnt vmcnt(27)
	v_lshlrev_b32_e32 v98, 16, v100
	v_and_b32_e32 v99, 0xffff0000, v100
	v_lshlrev_b32_e32 v100, 16, v101
	v_and_b32_e32 v101, 0xffff0000, v101
	v_pk_add_f32 v[98:99], v[66:67], v[98:99]
	v_pk_add_f32 v[82:83], v[82:83], v[100:101]
	global_load_dwordx2 v[100:101], v[28:29], off offset:-1024
	global_load_dwordx2 v[122:123], v[28:29], off offset:-512
	global_load_dwordx2 v[66:67], v[28:29], off
	v_pk_add_f32 v[48:49], v[82:83], v[48:49]
	v_pk_add_f32 v[82:83], v[98:99], v[124:125]
	v_pk_fma_f32 v[32:33], v[48:49], v[20:21], v[32:33]
	v_pk_fma_f32 v[18:19], v[82:83], v[18:19], v[30:31]
	v_lshlrev_b32_e32 v48, 16, v60
	v_bfe_u32 v20, v18, 16, 1
	v_add3_u32 v30, v18, v20, s37
	v_bfe_u32 v18, v19, 16, 1
	v_and_b32_sdwa v20, v33, v97 dst_sel:DWORD dst_unused:UNUSED_PAD src0_sel:WORD_1 src1_sel:DWORD
	v_add3_u32 v18, v19, v18, s37
	v_bfe_u32 v19, v32, 16, 1
	v_add3_u32 v20, v33, v20, s37
	v_and_b32_e32 v31, 0xffff0000, v18
	v_add3_u32 v19, v32, v19, s37
	v_and_b32_e32 v33, 0xffff0000, v20
	v_or_b32_sdwa v18, v31, v30 dst_sel:DWORD dst_unused:UNUSED_PAD src0_sel:DWORD src1_sel:WORD_1
	v_or_b32_sdwa v19, v33, v19 dst_sel:DWORD dst_unused:UNUSED_PAD src0_sel:DWORD src1_sel:WORD_1
	global_store_dwordx2 v[46:47], v[18:19], off
	global_load_dwordx4 v[18:21], v[26:27], off offset:1024
	v_and_b32_e32 v49, 0xffff0000, v60
	v_lshlrev_b32_e32 v60, 16, v61
	v_and_b32_e32 v61, 0xffff0000, v61
	v_pk_add_f32 v[48:49], v[48:49], 0 op_sel_hi:[1,0]
	v_pk_add_f32 v[60:61], v[60:61], 0 op_sel_hi:[1,0]
	s_waitcnt vmcnt(31)
	v_lshlrev_b32_e32 v82, 16, v102
	v_and_b32_e32 v83, 0xffff0000, v102
	v_lshlrev_b32_e32 v98, 16, v103
	v_and_b32_e32 v99, 0xffff0000, v103
	v_pk_add_f32 v[60:61], v[60:61], v[98:99]
	v_pk_add_f32 v[48:49], v[48:49], v[82:83]
	s_waitcnt vmcnt(28)
	v_lshlrev_b32_e32 v82, 16, v104
	v_and_b32_e32 v83, 0xffff0000, v104
	v_lshlrev_b32_e32 v98, 16, v105
	v_and_b32_e32 v99, 0xffff0000, v105
	v_pk_add_f32 v[48:49], v[48:49], v[82:83]
	v_pk_add_f32 v[60:61], v[60:61], v[98:99]
	s_waitcnt vmcnt(25)
	v_lshlrev_b32_e32 v82, 16, v106
	v_and_b32_e32 v83, 0xffff0000, v106
	v_lshlrev_b32_e32 v98, 16, v107
	v_and_b32_e32 v99, 0xffff0000, v107
	v_pk_add_f32 v[60:61], v[60:61], v[98:99]
	v_pk_add_f32 v[48:49], v[48:49], v[82:83]
	s_waitcnt vmcnt(22)
	v_lshlrev_b32_e32 v82, 16, v110
	v_and_b32_e32 v83, 0xffff0000, v110
	v_lshlrev_b32_e32 v98, 16, v111
	v_and_b32_e32 v99, 0xffff0000, v111
	v_pk_add_f32 v[48:49], v[48:49], v[82:83]
	v_pk_add_f32 v[60:61], v[60:61], v[98:99]
	s_waitcnt vmcnt(19)
	v_lshlrev_b32_e32 v82, 16, v112
	v_and_b32_e32 v83, 0xffff0000, v112
	v_lshlrev_b32_e32 v98, 16, v113
	v_and_b32_e32 v99, 0xffff0000, v113
	v_pk_add_f32 v[60:61], v[60:61], v[98:99]
	v_pk_add_f32 v[48:49], v[48:49], v[82:83]
	s_waitcnt vmcnt(16)
	v_lshlrev_b32_e32 v82, 16, v108
	v_and_b32_e32 v83, 0xffff0000, v108
	v_lshlrev_b32_e32 v98, 16, v109
	v_and_b32_e32 v99, 0xffff0000, v109
	v_pk_add_f32 v[48:49], v[48:49], v[82:83]
	v_pk_add_f32 v[60:61], v[60:61], v[98:99]
	s_waitcnt vmcnt(13)
	v_lshlrev_b32_e32 v82, 16, v116
	v_and_b32_e32 v83, 0xffff0000, v116
	v_lshlrev_b32_e32 v98, 16, v117
	v_and_b32_e32 v99, 0xffff0000, v117
	v_pk_add_f32 v[60:61], v[60:61], v[98:99]
	v_pk_add_f32 v[48:49], v[48:49], v[82:83]
	s_waitcnt vmcnt(10)
	v_lshlrev_b32_e32 v82, 16, v84
	v_and_b32_e32 v83, 0xffff0000, v84
	v_lshlrev_b32_e32 v84, 16, v85
	v_and_b32_e32 v85, 0xffff0000, v85
	v_pk_add_f32 v[48:49], v[48:49], v[82:83]
	v_pk_add_f32 v[60:61], v[60:61], v[84:85]
	s_waitcnt vmcnt(7)
	v_lshlrev_b32_e32 v82, 16, v80
	v_and_b32_e32 v83, 0xffff0000, v80
	v_lshlrev_b32_e32 v80, 16, v81
	v_and_b32_e32 v81, 0xffff0000, v81
	v_pk_add_f32 v[60:61], v[60:61], v[80:81]
	v_pk_add_f32 v[48:49], v[48:49], v[82:83]
	s_waitcnt vmcnt(4)
	v_lshlrev_b32_e32 v80, 16, v100
	v_and_b32_e32 v81, 0xffff0000, v100
	v_pk_add_f32 v[48:49], v[48:49], v[80:81]
	v_lshlrev_b32_e32 v82, 16, v101
	v_and_b32_e32 v83, 0xffff0000, v101
	v_pk_add_f32 v[60:61], v[60:61], v[82:83]
	v_lshl_add_u64 v[46:47], v[28:29], 0, s[16:17]
	v_lshlrev_b32_e32 v80, 16, v89
	v_and_b32_e32 v81, 0xffff0000, v89
	v_pk_add_f32 v[80:81], v[80:81], 0 op_sel_hi:[1,0]
	v_lshlrev_b32_e32 v82, 16, v90
	v_and_b32_e32 v83, 0xffff0000, v90
	v_lshlrev_b32_e32 v84, 16, v91
	v_and_b32_e32 v85, 0xffff0000, v91
	v_pk_add_f32 v[80:81], v[80:81], v[84:85]
	v_lshlrev_b32_e32 v84, 16, v93
	v_and_b32_e32 v85, 0xffff0000, v93
	v_pk_add_f32 v[80:81], v[80:81], v[84:85]
	v_and_b32_e32 v30, 0xffff0000, v30
	s_waitcnt vmcnt(0)
	v_pk_fma_f32 v[38:39], v[48:49], v[18:19], v[38:39]
	s_nop 0
	v_pk_fma_f32 v[34:35], v[60:61], v[20:21], v[34:35]
	v_and_b32_sdwa v20, v35, v97 dst_sel:DWORD dst_unused:UNUSED_PAD src0_sel:WORD_1 src1_sel:DWORD
	v_cvt_pk_bf16_f32 v18, v38, v39
	v_bfe_u32 v19, v34, 16, 1
	v_add3_u32 v20, v35, v20, s37
	v_add3_u32 v19, v34, v19, s37
	v_and_b32_e32 v35, 0xffff0000, v20
	v_or_b32_sdwa v19, v35, v19 dst_sel:DWORD dst_unused:UNUSED_PAD src0_sel:DWORD src1_sel:WORD_1
	global_store_dwordx2 v[46:47], v[18:19], off
	global_load_dwordx4 v[18:21], v[26:27], off offset:2048
	v_and_b32_sdwa v60, v32, v97 dst_sel:DWORD dst_unused:UNUSED_PAD src0_sel:WORD_1 src1_sel:DWORD
	v_add3_u32 v32, v32, v60, s37
	v_and_b32_sdwa v60, v39, v97 dst_sel:DWORD dst_unused:UNUSED_PAD src0_sel:WORD_1 src1_sel:DWORD
	v_and_b32_sdwa v61, v38, v97 dst_sel:DWORD dst_unused:UNUSED_PAD src0_sel:WORD_1 src1_sel:DWORD
	v_add3_u32 v39, v39, v60, s37
	v_add3_u32 v38, v38, v61, s37
	v_lshlrev_b32_e32 v60, 16, v88
	v_and_b32_e32 v61, 0xffff0000, v88
	v_pk_add_f32 v[60:61], v[60:61], 0 op_sel_hi:[1,0]
	v_lshl_add_u64 v[46:47], v[28:29], 0, s[18:19]
	v_pk_add_f32 v[60:61], v[60:61], v[82:83]
	v_lshlrev_b32_e32 v82, 16, v92
	v_and_b32_e32 v83, 0xffff0000, v92
	v_pk_add_f32 v[60:61], v[60:61], v[82:83]
	v_lshlrev_b32_e32 v82, 16, v72
	v_and_b32_e32 v83, 0xffff0000, v72
	v_lshlrev_b32_e32 v72, 16, v73
	v_and_b32_e32 v73, 0xffff0000, v73
	v_pk_add_f32 v[72:73], v[80:81], v[72:73]
	v_pk_add_f32 v[60:61], v[60:61], v[82:83]
	v_lshlrev_b32_e32 v80, 16, v70
	v_and_b32_e32 v81, 0xffff0000, v70
	v_lshlrev_b32_e32 v70, 16, v71
	v_and_b32_e32 v71, 0xffff0000, v71
	v_pk_add_f32 v[60:61], v[60:61], v[80:81]
	v_pk_add_f32 v[70:71], v[72:73], v[70:71]
	v_lshlrev_b32_e32 v72, 16, v68
	v_and_b32_e32 v73, 0xffff0000, v68
	v_lshlrev_b32_e32 v68, 16, v69
	v_and_b32_e32 v69, 0xffff0000, v69
	v_pk_add_f32 v[68:69], v[70:71], v[68:69]
	v_pk_add_f32 v[60:61], v[60:61], v[72:73]
	v_lshlrev_b32_e32 v70, 16, v114
	v_and_b32_e32 v71, 0xffff0000, v114
	v_pk_add_f32 v[60:61], v[60:61], v[70:71]
	v_lshlrev_b32_e32 v70, 16, v118
	v_and_b32_e32 v71, 0xffff0000, v118
	v_lshlrev_b32_e32 v72, 16, v115
	v_and_b32_e32 v73, 0xffff0000, v115
	v_pk_add_f32 v[60:61], v[60:61], v[70:71]
	v_lshlrev_b32_e32 v70, 16, v86
	v_and_b32_e32 v71, 0xffff0000, v86
	v_pk_add_f32 v[68:69], v[68:69], v[72:73]
	v_lshlrev_b32_e32 v72, 16, v119
	v_and_b32_e32 v73, 0xffff0000, v119
	v_pk_add_f32 v[60:61], v[60:61], v[70:71]
	v_lshlrev_b32_e32 v70, 16, v120
	v_and_b32_e32 v71, 0xffff0000, v120
	v_pk_add_f32 v[68:69], v[68:69], v[72:73]
	v_lshlrev_b32_e32 v72, 16, v87
	v_and_b32_e32 v73, 0xffff0000, v87
	v_pk_add_f32 v[60:61], v[60:61], v[70:71]
	v_lshlrev_b32_e32 v70, 16, v122
	v_and_b32_e32 v71, 0xffff0000, v122
	v_pk_add_f32 v[68:69], v[68:69], v[72:73]
	v_lshlrev_b32_e32 v72, 16, v121
	v_and_b32_e32 v73, 0xffff0000, v121
	v_pk_add_f32 v[60:61], v[60:61], v[70:71]
	v_pk_add_f32 v[68:69], v[68:69], v[72:73]
	v_lshlrev_b32_e32 v72, 16, v123
	v_and_b32_e32 v73, 0xffff0000, v123
	v_pk_add_f32 v[68:69], v[68:69], v[72:73]
	v_lshlrev_b32_e32 v70, 16, v75
	v_and_b32_e32 v71, 0xffff0000, v75
	v_lshl_add_u64 v[48:49], v[28:29], 0, s[20:21]
	v_and_b32_e32 v32, 0xffff0000, v32
	v_and_b32_e32 v39, 0xffff0000, v39
	v_and_b32_e32 v38, 0xffff0000, v38
	s_waitcnt vmcnt(0)
	v_pk_fma_f32 v[44:45], v[60:61], v[18:19], v[44:45]
	s_nop 0
	v_pk_fma_f32 v[40:41], v[68:69], v[20:21], v[40:41]
	v_and_b32_sdwa v20, v41, v97 dst_sel:DWORD dst_unused:UNUSED_PAD src0_sel:WORD_1 src1_sel:DWORD
	v_cvt_pk_bf16_f32 v18, v44, v45
	v_bfe_u32 v19, v40, 16, 1
	v_add3_u32 v20, v41, v20, s37
	v_add3_u32 v19, v40, v19, s37
	v_and_b32_e32 v41, 0xffff0000, v20
	v_or_b32_sdwa v19, v41, v19 dst_sel:DWORD dst_unused:UNUSED_PAD src0_sel:DWORD src1_sel:WORD_1
	global_store_dwordx2 v[46:47], v[18:19], off
	global_load_dwordx4 v[18:21], v[26:27], off offset:3072
	v_and_b32_sdwa v46, v34, v97 dst_sel:DWORD dst_unused:UNUSED_PAD src0_sel:WORD_1 src1_sel:DWORD
	v_add3_u32 v34, v34, v46, s37
	v_and_b32_sdwa v46, v45, v97 dst_sel:DWORD dst_unused:UNUSED_PAD src0_sel:WORD_1 src1_sel:DWORD
	v_and_b32_sdwa v47, v44, v97 dst_sel:DWORD dst_unused:UNUSED_PAD src0_sel:WORD_1 src1_sel:DWORD
	v_add3_u32 v45, v45, v46, s37
	v_add3_u32 v44, v44, v47, s37
	v_lshlrev_b32_e32 v46, 16, v76
	v_and_b32_e32 v47, 0xffff0000, v76
	v_lshlrev_b32_e32 v60, 16, v77
	v_and_b32_e32 v61, 0xffff0000, v77
	v_pk_add_f32 v[46:47], v[46:47], 0 op_sel_hi:[1,0]
	v_pk_add_f32 v[60:61], v[60:61], 0 op_sel_hi:[1,0]
	v_lshlrev_b32_e32 v68, 16, v74
	v_and_b32_e32 v69, 0xffff0000, v74
	v_pk_add_f32 v[60:61], v[60:61], v[70:71]
	v_pk_add_f32 v[46:47], v[46:47], v[68:69]
	v_lshlrev_b32_e32 v68, 16, v78
	v_and_b32_e32 v69, 0xffff0000, v78
	v_lshlrev_b32_e32 v70, 16, v79
	v_and_b32_e32 v71, 0xffff0000, v79
	v_pk_add_f32 v[46:47], v[46:47], v[68:69]
	v_pk_add_f32 v[60:61], v[60:61], v[70:71]
	v_lshlrev_b32_e32 v68, 16, v50
	v_and_b32_e32 v69, 0xffff0000, v50
	v_lshlrev_b32_e32 v50, 16, v51
	v_and_b32_e32 v51, 0xffff0000, v51
	v_pk_add_f32 v[50:51], v[60:61], v[50:51]
	v_pk_add_f32 v[46:47], v[46:47], v[68:69]
	v_lshlrev_b32_e32 v60, 16, v52
	v_and_b32_e32 v61, 0xffff0000, v52
	v_lshlrev_b32_e32 v52, 16, v53
	v_and_b32_e32 v53, 0xffff0000, v53
	v_pk_add_f32 v[46:47], v[46:47], v[60:61]
	v_pk_add_f32 v[50:51], v[50:51], v[52:53]
	v_lshlrev_b32_e32 v52, 16, v56
	v_and_b32_e32 v53, 0xffff0000, v56
	v_pk_add_f32 v[46:47], v[46:47], v[52:53]
	v_lshlrev_b32_e32 v52, 16, v54
	v_and_b32_e32 v53, 0xffff0000, v54
	v_pk_add_f32 v[46:47], v[46:47], v[52:53]
	v_lshlrev_b32_e32 v52, 16, v58
	v_and_b32_e32 v53, 0xffff0000, v58
	v_lshlrev_b32_e32 v56, 16, v57
	v_and_b32_e32 v57, 0xffff0000, v57
	v_pk_add_f32 v[46:47], v[46:47], v[52:53]
	v_lshlrev_b32_e32 v52, 16, v62
	v_and_b32_e32 v53, 0xffff0000, v62
	v_pk_add_f32 v[50:51], v[50:51], v[56:57]
	v_lshlrev_b32_e32 v54, 16, v55
	v_and_b32_e32 v55, 0xffff0000, v55
	v_pk_add_f32 v[46:47], v[46:47], v[52:53]
	v_lshlrev_b32_e32 v52, 16, v64
	v_and_b32_e32 v53, 0xffff0000, v64
	v_pk_add_f32 v[50:51], v[50:51], v[54:55]
	v_lshlrev_b32_e32 v54, 16, v59
	v_and_b32_e32 v55, 0xffff0000, v59
	v_pk_add_f32 v[46:47], v[46:47], v[52:53]
	v_lshlrev_b32_e32 v52, 16, v66
	v_and_b32_e32 v53, 0xffff0000, v66
	v_pk_add_f32 v[50:51], v[50:51], v[54:55]
	v_lshlrev_b32_e32 v54, 16, v63
	v_and_b32_e32 v55, 0xffff0000, v63
	v_pk_add_f32 v[46:47], v[46:47], v[52:53]
	v_pk_add_f32 v[50:51], v[50:51], v[54:55]
	v_lshlrev_b32_e32 v54, 16, v65
	v_and_b32_e32 v55, 0xffff0000, v65
	v_pk_add_f32 v[50:51], v[50:51], v[54:55]
	v_lshlrev_b32_e32 v54, 16, v67
	v_and_b32_e32 v55, 0xffff0000, v67
	v_pk_add_f32 v[50:51], v[50:51], v[54:55]
	v_and_b32_sdwa v52, v40, v97 dst_sel:DWORD dst_unused:UNUSED_PAD src0_sel:WORD_1 src1_sel:DWORD
	v_add3_u32 v40, v40, v52, s37
	v_and_b32_e32 v34, 0xffff0000, v34
	v_and_b32_e32 v45, 0xffff0000, v45
	v_and_b32_e32 v44, 0xffff0000, v44
	v_and_b32_e32 v40, 0xffff0000, v40
	s_waitcnt vmcnt(0)
	v_pk_fma_f32 v[18:19], v[46:47], v[18:19], v[36:37]
	s_nop 0
	v_pk_fma_f32 v[20:21], v[50:51], v[20:21], v[42:43]
	v_cvt_pk_bf16_f32 v46, v18, v19
	v_bfe_u32 v36, v20, 16, 1
	v_and_b32_sdwa v37, v18, v97 dst_sel:DWORD dst_unused:UNUSED_PAD src0_sel:WORD_1 src1_sel:DWORD
	v_add3_u32 v47, v20, v36, s37
	v_and_b32_sdwa v36, v19, v97 dst_sel:DWORD dst_unused:UNUSED_PAD src0_sel:WORD_1 src1_sel:DWORD
	v_add3_u32 v18, v18, v37, s37
	v_add3_u32 v19, v19, v36, s37
	v_and_b32_e32 v36, 0xffff0000, v18
	v_and_b32_sdwa v18, v21, v97 dst_sel:DWORD dst_unused:UNUSED_PAD src0_sel:WORD_1 src1_sel:DWORD
	v_and_b32_e32 v37, 0xffff0000, v19
	v_and_b32_sdwa v19, v20, v97 dst_sel:DWORD dst_unused:UNUSED_PAD src0_sel:WORD_1 src1_sel:DWORD
	v_add3_u32 v18, v21, v18, s37
	v_add3_u32 v19, v20, v19, s37
	v_and_b32_e32 v43, 0xffff0000, v18
	v_and_b32_e32 v42, 0xffff0000, v19
	v_or_b32_sdwa v47, v43, v47 dst_sel:DWORD dst_unused:UNUSED_PAD src0_sel:DWORD src1_sel:WORD_1
	global_store_dwordx2 v[48:49], v[46:47], off
	s_branch .LBB0_891

.LBB0_2013:
	s_cmp_lt_i32 s92, 27
	s_cselect_b64 s[4:5], -1, 0
	s_cmp_gt_i32 s93, 26
	s_cselect_b64 s[6:7], -1, 0
	s_and_b64 s[4:5], s[4:5], s[6:7]
	s_andn2_b64 vcc, exec, s[4:5]
	s_cbranch_vccnz .LBB0_2069
	s_lshl_b32 s3, s89, 3
	s_add_i32 s6, s3, s88
	s_cmpk_gt_i32 s6, 0x43ff
	s_mov_b32 s4, 7
	s_cbranch_scc1 .LBB0_2019
	s_ashr_i32 s5, s4, 31
	s_lshl_b32 s8, s34, 3
	s_lshl_b64 s[4:5], s[4:5], 3
	s_add_u32 s4, s0, s4
	s_addc_u32 s5, s1, s5
	s_load_dwordx2 s[4:5], s[4:5], 0x0
	s_waitcnt vmcnt(0)
	v_lshlrev_b32_e32 v24, 2, v250
	v_ashrrev_i32_e32 v25, 31, v24
	v_lshlrev_b64 v[18:19], 2, v[24:25]
	v_mbcnt_lo_u32_b32 v1, -1, 0
	s_waitcnt lgkmcnt(0)
	v_lshl_add_u64 v[2:3], s[4:5], 0, v[18:19]
	s_mov_b64 s[4:5], 0x2000
	v_lshl_add_u64 v[20:21], v[2:3], 0, s[4:5]
	v_add_co_u32_e32 v22, vcc, 0x2000, v2
	s_mov_b64 s[4:5], 0x13f000
	s_nop 0
	v_addc_co_u32_e32 v23, vcc, 0, v3, vcc
	global_load_dwordx4 v[2:5], v[20:21], off offset:1024
	global_load_dwordx4 v[6:9], v[20:21], off offset:2048
	global_load_dwordx4 v[10:13], v[22:23], off
	global_load_dwordx4 v[14:17], v[20:21], off offset:3072
	v_mbcnt_hi_u32_b32 v20, -1, v1
	v_and_b32_e32 v21, 64, v20
	v_xor_b32_e32 v1, 16, v20
	v_add_u32_e32 v21, 64, v21
	v_cmp_lt_i32_e32 vcc, v1, v21
	v_xor_b32_e32 v22, 32, v20
	s_ashr_i32 s7, s6, 31
	v_cndmask_b32_e32 v1, v20, v1, vcc
	v_cmp_lt_i32_e32 vcc, v22, v21
	s_mov_b32 s14, 0xdc9ffa00
	s_mov_b32 s16, 0xdc9ffc00
	v_cndmask_b32_e32 v20, v20, v22, vcc
	v_lshl_add_u64 v[22:23], s[26:27], 0, v[18:19]
	v_lshl_add_u64 v[18:19], v[22:23], 0, s[4:5]
	s_mov_b64 s[4:5], 0x140000
	v_lshlrev_b32_e32 v88, 2, v20
	v_lshl_add_u64 v[20:21], v[22:23], 0, s[4:5]
	s_mov_b64 s[4:5], 0x156000
	v_lshl_add_u64 v[22:23], v[22:23], 0, s[4:5]
	s_lshl_b64 s[4:5], s[6:7], 11
	s_add_u32 s4, s26, s4
	s_addc_u32 s5, s27, s5
	v_lshl_add_u64 v[24:25], v[24:25], 1, s[4:5]
	s_mov_b64 s[4:5], 0x3ed00600
	s_ashr_i32 s9, s8, 31
	s_mov_b32 s18, 0xdc9ffe00
	s_mov_b32 s20, 0xdca00000
	s_mov_b32 s11, 0
	v_lshlrev_b32_e32 v1, 2, v1
	v_lshl_add_u64 v[24:25], v[24:25], 0, s[4:5]
	s_lshl_b64 s[12:13], s[8:9], 11
	s_mov_b32 s15, -1
	s_mov_b32 s3, 0xffff0000
	s_mov_b32 s17, -1
	s_mov_b32 s19, -1
	s_mov_b32 s21, -1
	s_mov_b32 s7, 0xfec00000
	s_mov_b32 s9, 0xfee00000
	s_mov_b32 s22, 0xff000000
	s_mov_b32 s23, 0xff200000
	s_mov_b32 s30, 0xff400000
	s_mov_b32 s31, 0xff600000
	s_mov_b32 s33, 0xff800000
	s_mov_b32 s36, 0xffa00000
	s_mov_b32 s37, 0xffc00000
	s_mov_b32 s40, 0xffe00000
	s_movk_i32 s41, 0x7fff
	v_mov_b32_e32 v89, 0x358637bd
	s_mov_b32 s42, 0xf800000
	v_mov_b32_e32 v90, 0x260
	s_mov_b32 s43, 0xe0e00000
	v_mov_b32_e32 v91, 1
	v_add_co_u32_e32 v132, vcc, 0xdca00000, v24
	s_nop 1
	v_addc_co_u32_e32 v133, vcc, -1, v25, vcc
	global_load_dwordx2 v[136:137], v[132:133], off offset:-1536
	global_load_dwordx2 v[138:139], v[132:133], off offset:-1024
	global_load_dwordx2 v[140:141], v[132:133], off offset:-512
	global_load_dwordx2 v[142:143], v[132:133], off
	s_waitcnt vmcnt(0)
	s_branch .LBB0_2017
.LBB0_2016:
	v_pk_mul_f32 v[62:63], v[28:29], v[28:29]
	v_pk_mul_f32 v[64:65], v[26:27], v[26:27]
	v_pk_mul_f32 v[58:59], v[30:31], v[30:31]
	v_pk_mul_f32 v[60:61], v[32:33], v[32:33]
	v_pk_mov_b32 v[66:67], v[64:65], v[62:63] op_sel:[1,0]
	v_mov_b32_e32 v65, v63
	v_pk_add_f32 v[62:63], v[66:67], v[64:65]
	v_pk_mov_b32 v[64:65], v[60:61], v[58:59] op_sel:[1,0]
	v_mov_b32_e32 v61, v59
	v_pk_add_f32 v[58:59], v[64:65], v[60:61]
	s_add_i32 s10, s6, 0xfffffc00
	v_pk_add_f32 v[58:59], v[58:59], v[58:59] op_sel_hi:[0,1]
	v_mul_f32_e32 v58, v40, v40
	s_lshr_b32 s10, s10, 12
	v_pk_fma_f32 v[60:61], v[40:41], v[40:41], v[58:59] op_sel_hi:[1,1,0]
	v_mul_f32_e32 v58, v36, v36
	s_mulk_i32 s10, 0x1800
	s_and_b64 s[4:5], s[4:5], exec
	v_pk_add_f32 v[62:63], v[62:63], v[62:63] op_sel_hi:[0,1]
	v_pk_fma_f32 v[64:65], v[36:37], v[36:37], v[58:59] op_sel_hi:[1,1,0]
	s_cselect_b32 s10, 0x6000, s10
	v_mul_f32_e32 v60, v34, v34
	v_mul_f32_e32 v64, v35, v35
	v_mul_f32_e32 v62, v38, v38
	v_mul_f32_e32 v58, v39, v39
	s_lshl_b64 s[4:5], s[10:11], 2
	v_pk_add_f32 v[66:67], v[60:61], v[64:65]
	v_pk_add_f32 v[68:69], v[62:63], v[58:59]
	v_lshl_add_u64 v[54:55], v[20:21], 0, s[4:5]
	v_lshl_add_u64 v[70:71], v[18:19], 0, s[4:5]
	v_pk_add_f32 v[66:67], v[66:67], v[68:69]
	global_load_dwordx4 v[42:45], v[54:55], off
	global_load_dwordx4 v[46:49], v[54:55], off offset:1024
	global_load_dwordx4 v[50:53], v[54:55], off offset:2048
	s_nop 0
	global_load_dwordx4 v[54:57], v[54:55], off offset:3072
	s_nop 0
	global_load_dwordx4 v[58:61], v[70:71], off offset:2048
	global_load_dwordx4 v[62:65], v[70:71], off offset:3072
	v_add_f32_e32 v74, v66, v67
	global_load_dwordx4 v[66:69], v[70:71], off
	s_nop 0
	global_load_dwordx4 v[70:73], v[70:71], off offset:1024
	v_lshl_add_u64 v[132:133], v[132:133], 0, s[12:13]
	global_load_dwordx2 v[136:137], v[132:133], off offset:-1536
	global_load_dwordx2 v[138:139], v[132:133], off offset:-1024
	global_load_dwordx2 v[140:141], v[132:133], off offset:-512
	global_load_dwordx2 v[142:143], v[132:133], off
	v_add_f32_dpp v74, v74, v74 row_ror:8 row_mask:0xf bank_mask:0xf bound_ctrl:1
	s_add_i32 s6, s6, s8
	s_cmpk_lt_i32 s6, 0x4400
	v_add_f32_dpp v74, v74, v74 row_ror:4 row_mask:0xf bank_mask:0xf bound_ctrl:1
	s_waitcnt vmcnt(11)
	v_pk_add_f32 v[42:43], v[42:43], 1.0 op_sel_hi:[1,0]
	v_add_f32_dpp v74, v74, v74 row_ror:2 row_mask:0xf bank_mask:0xf bound_ctrl:1
	v_pk_add_f32 v[44:45], v[44:45], 1.0 op_sel_hi:[1,0]
	s_waitcnt vmcnt(10)
	v_pk_add_f32 v[46:47], v[46:47], 1.0 op_sel_hi:[1,0]
	v_add_f32_dpp v74, v74, v74 row_ror:1 row_mask:0xf bank_mask:0xf bound_ctrl:1
	v_mov_b32_e32 v75, v74
	s_nop 1
	v_permlane16_swap_b32_e32 v74, v75
	v_pk_add_f32 v[48:49], v[48:49], 1.0 op_sel_hi:[1,0]
	s_waitcnt vmcnt(9)
	v_pk_add_f32 v[50:51], v[50:51], 1.0 op_sel_hi:[1,0]
	v_pk_add_f32 v[52:53], v[52:53], 1.0 op_sel_hi:[1,0]
	s_waitcnt vmcnt(8)
	v_pk_add_f32 v[54:55], v[54:55], 1.0 op_sel_hi:[1,0]
	s_waitcnt lgkmcnt(0)
	v_add_f32_e32 v74, v74, v75
	v_mov_b32_e32 v75, v74
	s_nop 1
	v_permlane32_swap_b32_e32 v74, v75
	v_pk_add_f32 v[56:57], v[56:57], 1.0 op_sel_hi:[1,0]
	s_waitcnt lgkmcnt(0)
	v_add_f32_e32 v74, v74, v75
	v_fmamk_f32 v74, v74, 0x3a800000, v89
	v_mul_f32_e32 v75, 0x4f800000, v74
	v_cmp_gt_f32_e32 vcc, s42, v74
	s_nop 1
	v_cndmask_b32_e32 v74, v74, v75, vcc
	v_sqrt_f32_e32 v75, v74
	s_nop 0
	v_add_u32_e32 v76, -1, v75
	v_add_u32_e32 v77, 1, v75
	v_fma_f32 v78, -v76, v75, v74
	v_fma_f32 v79, -v77, v75, v74
	v_cmp_ge_f32_e64 s[4:5], 0, v78
	s_nop 1
	v_cndmask_b32_e64 v75, v75, v76, s[4:5]
	v_cmp_lt_f32_e64 s[4:5], 0, v79
	s_nop 1
	v_cndmask_b32_e64 v75, v75, v77, s[4:5]
	v_mul_f32_e32 v76, 0x37800000, v75
	v_cndmask_b32_e32 v75, v75, v76, vcc
	v_cmp_class_f32_e32 vcc, v74, v90
	s_nop 1
	v_cndmask_b32_e32 v74, v75, v74, vcc
	v_div_scale_f32 v75, s[4:5], v74, v74, 1.0
	v_rcp_f32_e32 v76, v75
	v_div_scale_f32 v77, vcc, 1.0, v74, 1.0
	v_fma_f32 v78, -v75, v76, 1.0
	v_fmac_f32_e32 v76, v78, v76
	v_mul_f32_e32 v78, v77, v76
	v_fma_f32 v79, -v75, v78, v77
	v_fmac_f32_e32 v78, v79, v76
	v_fma_f32 v75, -v75, v78, v77
	v_div_fmas_f32 v75, v75, v76, v78
	v_div_fixup_f32 v74, v75, v74, 1.0
	v_pk_mul_f32 v[26:27], v[26:27], v[74:75] op_sel_hi:[1,0]
	v_pk_mul_f32 v[28:29], v[28:29], v[74:75] op_sel_hi:[1,0]
	v_pk_mul_f32 v[26:27], v[10:11], v[26:27]
	v_pk_mul_f32 v[28:29], v[12:13], v[28:29]
	s_waitcnt vmcnt(5)
	v_pk_fma_f32 v[26:27], v[42:43], v[26:27], v[66:67]
	v_pk_fma_f32 v[28:29], v[44:45], v[28:29], v[68:69]
	v_bfe_u32 v42, v26, 16, 1
	v_add3_u32 v26, v26, v42, s41
	v_bfe_u32 v42, v27, 16, 1
	v_lshrrev_b32_e32 v26, 16, v26
	v_add3_u32 v27, v27, v42, s41
	v_and_or_b32 v26, v27, s3, v26
	v_bfe_u32 v27, v28, 16, 1
	v_add3_u32 v27, v28, v27, s41
	v_bfe_u32 v28, v29, 16, 1
	v_pk_mul_f32 v[32:33], v[32:33], v[74:75] op_sel_hi:[1,0]
	v_lshrrev_b32_e32 v27, 16, v27
	v_add3_u32 v28, v29, v28, s41
	v_pk_mul_f32 v[32:33], v[2:3], v[32:33]
	v_and_or_b32 v27, v28, s3, v27
	v_add_co_u32_e32 v28, vcc, s43, v24
	s_waitcnt vmcnt(4)
	v_pk_fma_f32 v[32:33], v[46:47], v[32:33], v[70:71]
	v_addc_co_u32_e32 v29, vcc, -1, v25, vcc
	v_pk_mul_f32 v[30:31], v[30:31], v[74:75] op_sel_hi:[1,0]
	global_store_dwordx2 v[28:29], v[26:27], off offset:-1536
	v_pk_mul_f32 v[30:31], v[4:5], v[30:31]
	v_pk_fma_f32 v[30:31], v[48:49], v[30:31], v[72:73]
	v_cvt_pk_bf16_f32 v26, v32, v33
	v_bfe_u32 v27, v30, 16, 1
	v_pk_mul_f32 v[40:41], v[40:41], v[74:75] op_sel_hi:[1,0]
	v_add3_u32 v27, v30, v27, s41
	v_bfe_u32 v30, v31, 16, 1
	v_pk_mul_f32 v[40:41], v[6:7], v[40:41]
	v_lshrrev_b32_e32 v27, 16, v27
	v_add3_u32 v30, v31, v30, s41
	v_pk_fma_f32 v[40:41], v[50:51], v[40:41], v[58:59]
	v_and_or_b32 v27, v30, s3, v27
	v_pk_mul_f32 v[36:37], v[36:37], v[74:75] op_sel_hi:[1,0]
	global_store_dwordx2 v[28:29], v[26:27], off offset:-1024
	v_pk_mul_f32 v[36:37], v[8:9], v[36:37]
	v_pk_fma_f32 v[36:37], v[52:53], v[36:37], v[60:61]
	v_cvt_pk_bf16_f32 v26, v40, v41
	v_pk_mul_f32 v[34:35], v[34:35], v[74:75] op_sel_hi:[1,0]
	v_pk_mul_f32 v[34:35], v[14:15], v[34:35]
	v_pk_fma_f32 v[34:35], v[54:55], v[34:35], v[62:63]
	v_cvt_pk_bf16_f32 v27, v36, v37
	v_pk_mul_f32 v[38:39], v[38:39], v[74:75] op_sel_hi:[1,0]
	global_store_dwordx2 v[28:29], v[26:27], off offset:-512
	v_pk_mul_f32 v[38:39], v[16:17], v[38:39]
	v_pk_fma_f32 v[38:39], v[56:57], v[38:39], v[64:65]
	v_cvt_pk_bf16_f32 v26, v34, v35
	v_cvt_pk_bf16_f32 v27, v38, v39
	v_lshl_add_u64 v[24:25], v[24:25], 0, s[12:13]
	global_store_dwordx2 v[28:29], v[26:27], off
	s_cbranch_scc0 .LBB0_2019
.LBB0_2017:
	s_waitcnt vmcnt(4)
	s_cmpk_lt_i32 s6, 0x400
	s_cselect_b64 s[4:5], -1, 0
	s_cmpk_gt_i32 s6, 0x3ff
	v_lshlrev_b32_e32 v26, 16, v136
	v_and_b32_e32 v27, 0xffff0000, v136
	v_lshlrev_b32_e32 v28, 16, v137
	v_and_b32_e32 v29, 0xffff0000, v137
	v_lshlrev_b32_e32 v32, 16, v138
	v_and_b32_e32 v33, 0xffff0000, v138
	v_lshlrev_b32_e32 v30, 16, v139
	v_and_b32_e32 v31, 0xffff0000, v139
	v_lshlrev_b32_e32 v40, 16, v140
	v_and_b32_e32 v41, 0xffff0000, v140
	v_lshlrev_b32_e32 v36, 16, v141
	v_and_b32_e32 v37, 0xffff0000, v141
	v_lshlrev_b32_e32 v34, 16, v142
	v_and_b32_e32 v35, 0xffff0000, v142
	v_lshlrev_b32_e32 v38, 16, v143
	v_and_b32_e32 v39, 0xffff0000, v143
	s_cbranch_scc1 .LBB0_2016
	v_add_co_u32_e32 v68, vcc, 0xfea00000, v24
	v_lshl_add_u64 v[42:43], v[24:25], 0, s[14:15]
	s_nop 0
	v_addc_co_u32_e32 v69, vcc, -1, v25, vcc
	v_add_co_u32_e32 v66, vcc, s7, v24
	global_load_dwordx2 v[46:47], v[68:69], off offset:-1536
	s_nop 0
	v_addc_co_u32_e32 v67, vcc, -1, v25, vcc
	global_load_dwordx2 v[64:65], v[66:67], off offset:-1536
	v_add_co_u32_e32 v60, vcc, s9, v24
	s_waitcnt vmcnt(1)
	v_lshlrev_b32_e32 v74, 16, v46
	v_addc_co_u32_e32 v61, vcc, -1, v25, vcc
	global_load_dwordx2 v[62:63], v[60:61], off offset:-1536
	v_add_co_u32_e32 v54, vcc, s22, v24
	v_and_b32_e32 v75, 0xffff0000, v46
	s_nop 0
	v_addc_co_u32_e32 v55, vcc, -1, v25, vcc
	v_add_co_u32_e32 v50, vcc, s23, v24
	global_load_dwordx2 v[58:59], v[54:55], off offset:-1536
	s_nop 0
	v_addc_co_u32_e32 v51, vcc, -1, v25, vcc
	v_add_co_u32_e32 v48, vcc, s30, v24
	global_load_dwordx2 v[56:57], v[50:51], off offset:-1536
	s_nop 0
	v_addc_co_u32_e32 v49, vcc, -1, v25, vcc
	v_add_co_u32_e32 v76, vcc, s31, v24
	global_load_dwordx2 v[52:53], v[48:49], off offset:-1536
	global_load_dwordx2 v[44:45], v[68:69], off offset:-1024
	global_load_dwordx2 v[70:71], v[68:69], off offset:-512
	s_nop 0
	global_load_dwordx2 v[68:69], v[68:69], off
	v_addc_co_u32_e32 v77, vcc, -1, v25, vcc
	v_add_co_u32_e32 v96, vcc, s33, v24
	global_load_dwordx2 v[86:87], v[76:77], off offset:-1536
	global_load_dwordx2 v[84:85], v[66:67], off offset:-1024
	global_load_dwordx2 v[72:73], v[66:67], off offset:-512
	s_nop 0
	global_load_dwordx2 v[66:67], v[66:67], off
	v_addc_co_u32_e32 v97, vcc, -1, v25, vcc
	v_add_co_u32_e32 v100, vcc, s36, v24
	global_load_dwordx2 v[98:99], v[96:97], off offset:-1536
	s_nop 0
	v_addc_co_u32_e32 v101, vcc, -1, v25, vcc
	v_add_co_u32_e32 v102, vcc, s37, v24
	global_load_dwordx2 v[104:105], v[100:101], off offset:-1536
	s_nop 0
	v_addc_co_u32_e32 v103, vcc, -1, v25, vcc
	v_add_co_u32_e32 v106, vcc, s40, v24
	global_load_dwordx2 v[108:109], v[102:103], off offset:-1536
	s_nop 0
	v_addc_co_u32_e32 v107, vcc, -1, v25, vcc
	v_lshlrev_b32_e32 v46, 16, v47
	v_and_b32_e32 v47, 0xffff0000, v47
	global_load_dwordx2 v[110:111], v[106:107], off offset:-1536
	v_pk_add_f32 v[46:47], v[46:47], 0 op_sel_hi:[1,0]
	s_waitcnt vmcnt(15)
	v_lshlrev_b32_e32 v78, 16, v64
	v_and_b32_e32 v79, 0xffff0000, v64
	v_lshlrev_b32_e32 v64, 16, v65
	v_and_b32_e32 v65, 0xffff0000, v65
	v_pk_add_f32 v[80:81], v[46:47], v[64:65]
	global_load_dwordx2 v[112:113], v[60:61], off offset:-1024
	global_load_dwordx2 v[64:65], v[60:61], off offset:-512
	global_load_dwordx2 v[46:47], v[60:61], off
	global_load_dwordx2 v[114:115], v[24:25], off offset:-1536
	v_pk_add_f32 v[74:75], v[74:75], 0 op_sel_hi:[1,0]
	s_waitcnt vmcnt(18)
	v_lshlrev_b32_e32 v60, 16, v62
	v_pk_add_f32 v[74:75], v[74:75], v[78:79]
	v_and_b32_e32 v61, 0xffff0000, v62
	v_pk_add_f32 v[60:61], v[74:75], v[60:61]
	global_load_dwordx4 v[92:95], v[22:23], off
	global_load_dwordx2 v[116:117], v[54:55], off offset:-1024
	global_load_dwordx2 v[74:75], v[54:55], off offset:-512
	s_nop 0
	global_load_dwordx2 v[54:55], v[54:55], off
	v_lshlrev_b32_e32 v62, 16, v63
	v_and_b32_e32 v63, 0xffff0000, v63
	v_pk_add_f32 v[62:63], v[80:81], v[62:63]
	s_waitcnt vmcnt(21)
	v_lshlrev_b32_e32 v78, 16, v58
	v_and_b32_e32 v79, 0xffff0000, v58
	v_lshlrev_b32_e32 v58, 16, v59
	v_and_b32_e32 v59, 0xffff0000, v59
	v_pk_add_f32 v[58:59], v[62:63], v[58:59]
	v_pk_add_f32 v[60:61], v[60:61], v[78:79]
	s_waitcnt vmcnt(20)
	v_lshlrev_b32_e32 v62, 16, v56
	v_and_b32_e32 v63, 0xffff0000, v56
	v_lshlrev_b32_e32 v56, 16, v57
	v_and_b32_e32 v57, 0xffff0000, v57
	v_pk_add_f32 v[60:61], v[60:61], v[62:63]
	v_pk_add_f32 v[56:57], v[58:59], v[56:57]
	s_waitcnt vmcnt(19)
	v_lshlrev_b32_e32 v58, 16, v52
	v_and_b32_e32 v59, 0xffff0000, v52
	v_lshlrev_b32_e32 v52, 16, v53
	v_and_b32_e32 v53, 0xffff0000, v53
	v_pk_add_f32 v[56:57], v[56:57], v[52:53]
	v_pk_add_f32 v[58:59], v[60:61], v[58:59]
	s_waitcnt vmcnt(15)
	v_lshlrev_b32_e32 v60, 16, v86
	v_and_b32_e32 v61, 0xffff0000, v86
	v_lshlrev_b32_e32 v62, 16, v87
	v_and_b32_e32 v63, 0xffff0000, v87
	global_load_dwordx2 v[118:119], v[50:51], off offset:-1024
	global_load_dwordx2 v[78:79], v[50:51], off offset:-512
	s_nop 0
	global_load_dwordx2 v[50:51], v[50:51], off
	s_nop 0
	global_load_dwordx2 v[120:121], v[48:49], off offset:-1024
	global_load_dwordx2 v[80:81], v[48:49], off offset:-512
	s_nop 0
	global_load_dwordx2 v[48:49], v[48:49], off
	s_nop 0
	global_load_dwordx2 v[122:123], v[76:77], off offset:-1024
	global_load_dwordx2 v[82:83], v[76:77], off offset:-512
	global_load_dwordx2 v[52:53], v[76:77], off
	v_pk_add_f32 v[58:59], v[58:59], v[60:61]
	v_pk_add_f32 v[60:61], v[56:57], v[62:63]
	s_waitcnt vmcnt(20)
	v_lshlrev_b32_e32 v62, 16, v98
	v_and_b32_e32 v63, 0xffff0000, v98
	v_lshlrev_b32_e32 v76, 16, v99
	v_and_b32_e32 v77, 0xffff0000, v99
	global_load_dwordx2 v[124:125], v[96:97], off offset:-1024
	global_load_dwordx2 v[86:87], v[96:97], off offset:-512
	global_load_dwordx2 v[56:57], v[96:97], off
	v_pk_add_f32 v[60:61], v[60:61], v[76:77]
	v_pk_add_f32 v[62:63], v[58:59], v[62:63]
	global_load_dwordx2 v[96:97], v[100:101], off offset:-1024
	global_load_dwordx2 v[98:99], v[100:101], off offset:-512
	global_load_dwordx2 v[58:59], v[100:101], off
	s_waitcnt vmcnt(25)
	v_lshlrev_b32_e32 v76, 16, v104
	v_and_b32_e32 v77, 0xffff0000, v104
	v_lshlrev_b32_e32 v100, 16, v105
	v_and_b32_e32 v101, 0xffff0000, v105
	v_pk_add_f32 v[62:63], v[62:63], v[76:77]
	v_pk_add_f32 v[76:77], v[60:61], v[100:101]
	global_load_dwordx2 v[100:101], v[102:103], off offset:-1024
	global_load_dwordx2 v[104:105], v[102:103], off offset:-512
	global_load_dwordx2 v[60:61], v[102:103], off
	s_waitcnt vmcnt(27)
	v_lshlrev_b32_e32 v102, 16, v108
	v_and_b32_e32 v103, 0xffff0000, v108
	v_lshlrev_b32_e32 v108, 16, v109
	v_and_b32_e32 v109, 0xffff0000, v109
	v_pk_add_f32 v[76:77], v[76:77], v[108:109]
	v_pk_add_f32 v[102:103], v[62:63], v[102:103]
	global_load_dwordx2 v[108:109], v[106:107], off offset:-1024
	global_load_dwordx2 v[126:127], v[106:107], off offset:-512
	global_load_dwordx2 v[62:63], v[106:107], off
	s_waitcnt vmcnt(29)
	v_lshlrev_b32_e32 v106, 16, v110
	v_and_b32_e32 v107, 0xffff0000, v110
	v_lshlrev_b32_e32 v110, 16, v111
	v_and_b32_e32 v111, 0xffff0000, v111
	v_pk_add_f32 v[102:103], v[102:103], v[106:107]
	s_waitcnt vmcnt(25)
	v_lshlrev_b32_e32 v130, 16, v114
	v_and_b32_e32 v131, 0xffff0000, v114
	v_pk_add_f32 v[106:107], v[76:77], v[110:111]
	v_lshlrev_b32_e32 v114, 16, v115
	v_and_b32_e32 v115, 0xffff0000, v115
	v_pk_add_f32 v[102:103], v[102:103], v[130:131]
	v_pk_add_f32 v[106:107], v[106:107], v[114:115]
	global_load_dwordx2 v[110:111], v[24:25], off offset:-1024
	global_load_dwordx2 v[128:129], v[24:25], off offset:-512
	global_load_dwordx2 v[76:77], v[24:25], off
	v_lshlrev_b32_e32 v114, 16, v44
	v_and_b32_e32 v115, 0xffff0000, v44
	v_lshlrev_b32_e32 v44, 16, v45
	v_and_b32_e32 v45, 0xffff0000, v45
	v_pk_add_f32 v[44:45], v[44:45], 0 op_sel_hi:[1,0]
	v_pk_add_f32 v[114:115], v[114:115], 0 op_sel_hi:[1,0]
	v_lshlrev_b32_e32 v130, 16, v84
	v_and_b32_e32 v131, 0xffff0000, v84
	v_lshlrev_b32_e32 v84, 16, v85
	v_and_b32_e32 v85, 0xffff0000, v85
	v_pk_add_f32 v[114:115], v[114:115], v[130:131]
	s_waitcnt vmcnt(27)
	v_pk_fma_f32 v[26:27], v[102:103], v[92:93], v[26:27]
	v_pk_fma_f32 v[28:29], v[106:107], v[94:95], v[28:29]
	v_bfe_u32 v92, v26, 16, 1
	v_add3_u32 v26, v26, v92, s41
	v_bfe_u32 v92, v27, 16, 1
	v_and_b32_sdwa v94, v29, v91 dst_sel:DWORD dst_unused:UNUSED_PAD src0_sel:WORD_1 src1_sel:DWORD
	v_add3_u32 v27, v27, v92, s41
	v_bfe_u32 v93, v28, 16, 1
	v_add3_u32 v29, v29, v94, s41
	v_and_b32_e32 v27, 0xffff0000, v27
	v_add3_u32 v93, v28, v93, s41
	v_and_b32_e32 v29, 0xffff0000, v29
	v_or_b32_sdwa v92, v27, v26 dst_sel:DWORD dst_unused:UNUSED_PAD src0_sel:DWORD src1_sel:WORD_1
	v_or_b32_sdwa v93, v29, v93 dst_sel:DWORD dst_unused:UNUSED_PAD src0_sel:DWORD src1_sel:WORD_1
	global_store_dwordx2 v[42:43], v[92:93], off
	global_load_dwordx4 v[92:95], v[22:23], off offset:1024
	v_pk_add_f32 v[44:45], v[44:45], v[84:85]
	v_lshlrev_b32_e32 v84, 16, v112
	v_and_b32_e32 v85, 0xffff0000, v112
	v_lshlrev_b32_e32 v112, 16, v113
	v_and_b32_e32 v113, 0xffff0000, v113
	v_pk_add_f32 v[44:45], v[44:45], v[112:113]
	v_pk_add_f32 v[84:85], v[114:115], v[84:85]
	s_waitcnt vmcnt(28)
	v_lshlrev_b32_e32 v112, 16, v116
	v_and_b32_e32 v113, 0xffff0000, v116
	v_lshlrev_b32_e32 v114, 16, v117
	v_and_b32_e32 v115, 0xffff0000, v117
	v_pk_add_f32 v[84:85], v[84:85], v[112:113]
	v_pk_add_f32 v[44:45], v[44:45], v[114:115]
	s_waitcnt vmcnt(25)
	v_lshlrev_b32_e32 v112, 16, v118
	v_and_b32_e32 v113, 0xffff0000, v118
	v_lshlrev_b32_e32 v114, 16, v119
	v_and_b32_e32 v115, 0xffff0000, v119
	v_pk_add_f32 v[44:45], v[44:45], v[114:115]
	v_pk_add_f32 v[84:85], v[84:85], v[112:113]
	s_waitcnt vmcnt(22)
	v_lshlrev_b32_e32 v112, 16, v120
	v_and_b32_e32 v113, 0xffff0000, v120
	v_lshlrev_b32_e32 v114, 16, v121
	v_and_b32_e32 v115, 0xffff0000, v121
	v_pk_add_f32 v[84:85], v[84:85], v[112:113]
	v_pk_add_f32 v[44:45], v[44:45], v[114:115]
	s_waitcnt vmcnt(19)
	v_lshlrev_b32_e32 v112, 16, v122
	v_and_b32_e32 v113, 0xffff0000, v122
	v_lshlrev_b32_e32 v114, 16, v123
	v_and_b32_e32 v115, 0xffff0000, v123
	v_pk_add_f32 v[44:45], v[44:45], v[114:115]
	v_pk_add_f32 v[84:85], v[84:85], v[112:113]
	s_waitcnt vmcnt(16)
	v_lshlrev_b32_e32 v112, 16, v124
	v_and_b32_e32 v113, 0xffff0000, v124
	v_lshlrev_b32_e32 v114, 16, v125
	v_and_b32_e32 v115, 0xffff0000, v125
	v_pk_add_f32 v[84:85], v[84:85], v[112:113]
	v_pk_add_f32 v[44:45], v[44:45], v[114:115]
	s_waitcnt vmcnt(13)
	v_lshlrev_b32_e32 v112, 16, v96
	v_and_b32_e32 v113, 0xffff0000, v96
	v_lshlrev_b32_e32 v96, 16, v97
	v_and_b32_e32 v97, 0xffff0000, v97
	v_pk_add_f32 v[44:45], v[44:45], v[96:97]
	v_pk_add_f32 v[84:85], v[84:85], v[112:113]
	s_waitcnt vmcnt(10)
	v_lshlrev_b32_e32 v96, 16, v100
	v_and_b32_e32 v97, 0xffff0000, v100
	v_lshlrev_b32_e32 v100, 16, v101
	v_and_b32_e32 v101, 0xffff0000, v101
	v_pk_add_f32 v[84:85], v[84:85], v[96:97]
	s_waitcnt vmcnt(7)
	v_lshlrev_b32_e32 v96, 16, v108
	v_and_b32_e32 v97, 0xffff0000, v108
	v_pk_add_f32 v[44:45], v[44:45], v[100:101]
	v_lshlrev_b32_e32 v100, 16, v109
	v_and_b32_e32 v101, 0xffff0000, v109
	v_pk_add_f32 v[84:85], v[84:85], v[96:97]
	s_waitcnt vmcnt(4)
	v_lshlrev_b32_e32 v96, 16, v110
	v_and_b32_e32 v97, 0xffff0000, v110
	v_pk_add_f32 v[44:45], v[44:45], v[100:101]
	v_lshlrev_b32_e32 v100, 16, v111
	v_and_b32_e32 v101, 0xffff0000, v111
	v_pk_add_f32 v[84:85], v[84:85], v[96:97]
	v_pk_add_f32 v[44:45], v[44:45], v[100:101]
	v_lshl_add_u64 v[102:103], v[24:25], 0, s[16:17]
	v_lshl_add_u64 v[106:107], v[24:25], 0, s[18:19]
	v_and_b32_sdwa v96, v28, v91 dst_sel:DWORD dst_unused:UNUSED_PAD src0_sel:WORD_1 src1_sel:DWORD
	v_add3_u32 v28, v28, v96, s41
	v_lshl_add_u64 v[42:43], v[24:25], 0, s[20:21]
	v_and_b32_e32 v26, 0xffff0000, v26
	v_and_b32_e32 v28, 0xffff0000, v28
	s_waitcnt vmcnt(0)
	v_pk_fma_f32 v[32:33], v[84:85], v[92:93], v[32:33]
	v_pk_fma_f32 v[30:31], v[44:45], v[94:95], v[30:31]
	v_and_b32_sdwa v92, v31, v91 dst_sel:DWORD dst_unused:UNUSED_PAD src0_sel:WORD_1 src1_sel:DWORD
	v_cvt_pk_bf16_f32 v44, v32, v33
	v_bfe_u32 v45, v30, 16, 1
	v_add3_u32 v31, v31, v92, s41
	v_add3_u32 v45, v30, v45, s41
	v_and_b32_e32 v31, 0xffff0000, v31
	v_or_b32_sdwa v45, v31, v45 dst_sel:DWORD dst_unused:UNUSED_PAD src0_sel:DWORD src1_sel:WORD_1
	global_store_dwordx2 v[102:103], v[44:45], off
	global_load_dwordx4 v[92:95], v[22:23], off offset:2048
	v_and_b32_sdwa v84, v33, v91 dst_sel:DWORD dst_unused:UNUSED_PAD src0_sel:WORD_1 src1_sel:DWORD
	v_and_b32_sdwa v85, v32, v91 dst_sel:DWORD dst_unused:UNUSED_PAD src0_sel:WORD_1 src1_sel:DWORD
	v_lshlrev_b32_e32 v44, 16, v70
	v_and_b32_e32 v45, 0xffff0000, v70
	v_lshlrev_b32_e32 v70, 16, v71
	v_and_b32_e32 v71, 0xffff0000, v71
	v_add3_u32 v33, v33, v84, s41
	v_add3_u32 v32, v32, v85, s41
	v_pk_add_f32 v[70:71], v[70:71], 0 op_sel_hi:[1,0]
	v_pk_add_f32 v[44:45], v[44:45], 0 op_sel_hi:[1,0]
	v_lshlrev_b32_e32 v84, 16, v72
	v_and_b32_e32 v85, 0xffff0000, v72
	v_lshlrev_b32_e32 v72, 16, v73
	v_and_b32_e32 v73, 0xffff0000, v73
	v_pk_add_f32 v[44:45], v[44:45], v[84:85]
	v_pk_add_f32 v[70:71], v[70:71], v[72:73]
	v_lshlrev_b32_e32 v72, 16, v64
	v_and_b32_e32 v73, 0xffff0000, v64
	v_lshlrev_b32_e32 v64, 16, v65
	v_and_b32_e32 v65, 0xffff0000, v65
	v_pk_add_f32 v[64:65], v[70:71], v[64:65]
	v_pk_add_f32 v[44:45], v[44:45], v[72:73]
	v_lshlrev_b32_e32 v70, 16, v74
	v_and_b32_e32 v71, 0xffff0000, v74
	v_pk_add_f32 v[44:45], v[44:45], v[70:71]
	v_lshlrev_b32_e32 v70, 16, v78
	v_and_b32_e32 v71, 0xffff0000, v78
	v_lshlrev_b32_e32 v72, 16, v75
	v_and_b32_e32 v73, 0xffff0000, v75
	v_pk_add_f32 v[44:45], v[44:45], v[70:71]
	v_lshlrev_b32_e32 v70, 16, v80
	v_and_b32_e32 v71, 0xffff0000, v80
	v_pk_add_f32 v[64:65], v[64:65], v[72:73]
	v_lshlrev_b32_e32 v72, 16, v79
	v_and_b32_e32 v73, 0xffff0000, v79
	v_pk_add_f32 v[44:45], v[44:45], v[70:71]
	v_lshlrev_b32_e32 v70, 16, v82
	v_and_b32_e32 v71, 0xffff0000, v82
	v_pk_add_f32 v[64:65], v[64:65], v[72:73]
	v_lshlrev_b32_e32 v72, 16, v81
	v_and_b32_e32 v73, 0xffff0000, v81
	v_pk_add_f32 v[44:45], v[44:45], v[70:71]
	v_lshlrev_b32_e32 v70, 16, v86
	v_and_b32_e32 v71, 0xffff0000, v86
	v_pk_add_f32 v[64:65], v[64:65], v[72:73]
	v_lshlrev_b32_e32 v72, 16, v83
	v_and_b32_e32 v73, 0xffff0000, v83
	v_pk_add_f32 v[44:45], v[44:45], v[70:71]
	v_lshlrev_b32_e32 v70, 16, v98
	v_and_b32_e32 v71, 0xffff0000, v98
	v_pk_add_f32 v[64:65], v[64:65], v[72:73]
	v_lshlrev_b32_e32 v72, 16, v87
	v_and_b32_e32 v73, 0xffff0000, v87
	v_pk_add_f32 v[44:45], v[44:45], v[70:71]
	v_lshlrev_b32_e32 v70, 16, v104
	v_and_b32_e32 v71, 0xffff0000, v104
	v_pk_add_f32 v[64:65], v[64:65], v[72:73]
	v_lshlrev_b32_e32 v72, 16, v99
	v_and_b32_e32 v73, 0xffff0000, v99
	v_pk_add_f32 v[44:45], v[44:45], v[70:71]
	v_lshlrev_b32_e32 v70, 16, v126
	v_and_b32_e32 v71, 0xffff0000, v126
	v_pk_add_f32 v[64:65], v[64:65], v[72:73]
	v_lshlrev_b32_e32 v72, 16, v105
	v_and_b32_e32 v73, 0xffff0000, v105
	v_pk_add_f32 v[44:45], v[44:45], v[70:71]
	v_lshlrev_b32_e32 v70, 16, v128
	v_and_b32_e32 v71, 0xffff0000, v128
	v_pk_add_f32 v[64:65], v[64:65], v[72:73]
	v_lshlrev_b32_e32 v72, 16, v127
	v_and_b32_e32 v73, 0xffff0000, v127
	v_pk_add_f32 v[44:45], v[44:45], v[70:71]
	v_pk_add_f32 v[64:65], v[64:65], v[72:73]
	v_lshlrev_b32_e32 v72, 16, v129
	v_and_b32_e32 v73, 0xffff0000, v129
	v_pk_add_f32 v[64:65], v[64:65], v[72:73]
	v_and_b32_sdwa v70, v30, v91 dst_sel:DWORD dst_unused:UNUSED_PAD src0_sel:WORD_1 src1_sel:DWORD
	v_add3_u32 v30, v30, v70, s41
	v_and_b32_e32 v33, 0xffff0000, v33
	s_waitcnt vmcnt(0)
	v_pk_fma_f32 v[40:41], v[44:45], v[92:93], v[40:41]
	v_pk_fma_f32 v[36:37], v[64:65], v[94:95], v[36:37]
	v_and_b32_sdwa v70, v37, v91 dst_sel:DWORD dst_unused:UNUSED_PAD src0_sel:WORD_1 src1_sel:DWORD
	v_cvt_pk_bf16_f32 v44, v40, v41
	v_bfe_u32 v45, v36, 16, 1
	v_add3_u32 v37, v37, v70, s41
	v_add3_u32 v45, v36, v45, s41
	v_and_b32_e32 v37, 0xffff0000, v37
	v_or_b32_sdwa v45, v37, v45 dst_sel:DWORD dst_unused:UNUSED_PAD src0_sel:DWORD src1_sel:WORD_1
	global_store_dwordx2 v[106:107], v[44:45], off
	global_load_dwordx4 v[70:73], v[22:23], off offset:3072
	v_and_b32_sdwa v64, v41, v91 dst_sel:DWORD dst_unused:UNUSED_PAD src0_sel:WORD_1 src1_sel:DWORD
	v_and_b32_sdwa v65, v40, v91 dst_sel:DWORD dst_unused:UNUSED_PAD src0_sel:WORD_1 src1_sel:DWORD
	v_add3_u32 v41, v41, v64, s41
	v_add3_u32 v40, v40, v65, s41
	v_lshlrev_b32_e32 v44, 16, v68
	v_and_b32_e32 v45, 0xffff0000, v68
	v_lshlrev_b32_e32 v64, 16, v69
	v_and_b32_e32 v65, 0xffff0000, v69
	v_pk_add_f32 v[64:65], v[64:65], 0 op_sel_hi:[1,0]
	v_pk_add_f32 v[44:45], v[44:45], 0 op_sel_hi:[1,0]
	v_lshlrev_b32_e32 v68, 16, v66
	v_and_b32_e32 v69, 0xffff0000, v66
	v_lshlrev_b32_e32 v66, 16, v67
	v_and_b32_e32 v67, 0xffff0000, v67
	v_pk_add_f32 v[44:45], v[44:45], v[68:69]
	v_pk_add_f32 v[64:65], v[64:65], v[66:67]
	v_lshlrev_b32_e32 v66, 16, v46
	v_and_b32_e32 v67, 0xffff0000, v46
	v_lshlrev_b32_e32 v46, 16, v47
	v_and_b32_e32 v47, 0xffff0000, v47
	v_pk_add_f32 v[46:47], v[64:65], v[46:47]
	v_pk_add_f32 v[44:45], v[44:45], v[66:67]
	v_lshlrev_b32_e32 v64, 16, v54
	v_and_b32_e32 v65, 0xffff0000, v54
	v_lshlrev_b32_e32 v54, 16, v55
	v_and_b32_e32 v55, 0xffff0000, v55
	v_pk_add_f32 v[44:45], v[44:45], v[64:65]
	v_pk_add_f32 v[46:47], v[46:47], v[54:55]
	v_lshlrev_b32_e32 v54, 16, v50
	v_and_b32_e32 v55, 0xffff0000, v50
	v_lshlrev_b32_e32 v50, 16, v51
	v_and_b32_e32 v51, 0xffff0000, v51
	v_pk_add_f32 v[46:47], v[46:47], v[50:51]
	v_pk_add_f32 v[44:45], v[44:45], v[54:55]
	v_lshlrev_b32_e32 v50, 16, v48
	v_and_b32_e32 v51, 0xffff0000, v48
	v_lshlrev_b32_e32 v48, 16, v49
	v_and_b32_e32 v49, 0xffff0000, v49
	v_pk_add_f32 v[44:45], v[44:45], v[50:51]
	v_pk_add_f32 v[46:47], v[46:47], v[48:49]
	v_lshlrev_b32_e32 v48, 16, v52
	v_and_b32_e32 v49, 0xffff0000, v52
	v_pk_add_f32 v[44:45], v[44:45], v[48:49]
	v_lshlrev_b32_e32 v48, 16, v56
	v_and_b32_e32 v49, 0xffff0000, v56
	v_lshlrev_b32_e32 v50, 16, v53
	v_and_b32_e32 v51, 0xffff0000, v53
	v_pk_add_f32 v[44:45], v[44:45], v[48:49]
	v_lshlrev_b32_e32 v48, 16, v58
	v_and_b32_e32 v49, 0xffff0000, v58
	v_pk_add_f32 v[46:47], v[46:47], v[50:51]
	v_lshlrev_b32_e32 v50, 16, v57
	v_and_b32_e32 v51, 0xffff0000, v57
	v_pk_add_f32 v[44:45], v[44:45], v[48:49]
	v_lshlrev_b32_e32 v48, 16, v60
	v_and_b32_e32 v49, 0xffff0000, v60
	v_pk_add_f32 v[46:47], v[46:47], v[50:51]
	v_lshlrev_b32_e32 v50, 16, v59
	v_and_b32_e32 v51, 0xffff0000, v59
	v_pk_add_f32 v[44:45], v[44:45], v[48:49]
	v_lshlrev_b32_e32 v48, 16, v62
	v_and_b32_e32 v49, 0xffff0000, v62
	v_pk_add_f32 v[46:47], v[46:47], v[50:51]
	v_lshlrev_b32_e32 v50, 16, v61
	v_and_b32_e32 v51, 0xffff0000, v61
	v_pk_add_f32 v[44:45], v[44:45], v[48:49]
	v_lshlrev_b32_e32 v48, 16, v76
	v_and_b32_e32 v49, 0xffff0000, v76
	v_pk_add_f32 v[46:47], v[46:47], v[50:51]
	v_lshlrev_b32_e32 v50, 16, v63
	v_and_b32_e32 v51, 0xffff0000, v63
	v_pk_add_f32 v[44:45], v[44:45], v[48:49]
	v_pk_add_f32 v[46:47], v[46:47], v[50:51]
	v_lshlrev_b32_e32 v50, 16, v77
	v_and_b32_e32 v51, 0xffff0000, v77
	v_pk_add_f32 v[46:47], v[46:47], v[50:51]
	v_and_b32_sdwa v48, v36, v91 dst_sel:DWORD dst_unused:UNUSED_PAD src0_sel:WORD_1 src1_sel:DWORD
	v_add3_u32 v36, v36, v48, s41
	v_and_b32_e32 v32, 0xffff0000, v32
	s_waitcnt vmcnt(0)
	v_pk_fma_f32 v[34:35], v[44:45], v[70:71], v[34:35]
	v_pk_fma_f32 v[38:39], v[46:47], v[72:73], v[38:39]
	v_bfe_u32 v44, v34, 16, 1
	v_add3_u32 v44, v34, v44, s41
	v_bfe_u32 v45, v35, 16, 1
	v_and_b32_sdwa v46, v35, v91 dst_sel:DWORD dst_unused:UNUSED_PAD src0_sel:WORD_1 src1_sel:DWORD
	v_lshrrev_b32_e32 v44, 16, v44
	v_add3_u32 v45, v35, v45, s41
	v_and_b32_sdwa v47, v34, v91 dst_sel:DWORD dst_unused:UNUSED_PAD src0_sel:WORD_1 src1_sel:DWORD
	v_add3_u32 v35, v35, v46, s41
	v_and_b32_sdwa v46, v39, v91 dst_sel:DWORD dst_unused:UNUSED_PAD src0_sel:WORD_1 src1_sel:DWORD
	v_and_or_b32 v44, v45, s3, v44
	v_bfe_u32 v45, v38, 16, 1
	v_add3_u32 v34, v34, v47, s41
	v_and_b32_sdwa v47, v38, v91 dst_sel:DWORD dst_unused:UNUSED_PAD src0_sel:WORD_1 src1_sel:DWORD
	v_add3_u32 v39, v39, v46, s41
	v_add3_u32 v45, v38, v45, s41
	v_add3_u32 v38, v38, v47, s41
	v_and_b32_e32 v39, 0xffff0000, v39
	v_and_b32_e32 v30, 0xffff0000, v30
	v_and_b32_e32 v41, 0xffff0000, v41
	v_and_b32_e32 v40, 0xffff0000, v40
	v_and_b32_e32 v36, 0xffff0000, v36
	v_and_b32_e32 v35, 0xffff0000, v35
	v_and_b32_e32 v34, 0xffff0000, v34
	v_and_b32_e32 v38, 0xffff0000, v38
	v_or_b32_sdwa v45, v39, v45 dst_sel:DWORD dst_unused:UNUSED_PAD src0_sel:DWORD src1_sel:WORD_1
	global_store_dwordx2 v[42:43], v[44:45], off
	s_branch .LBB0_2016

.LBB0_2228:
	s_cmp_lt_i32 s92, 30
	s_cselect_b64 s[4:5], -1, 0
	s_cmp_gt_i32 s93, 29
	s_cselect_b64 s[6:7], -1, 0
	s_and_b64 s[4:5], s[4:5], s[6:7]
	s_andn2_b64 vcc, exec, s[4:5]
	s_cbranch_vccnz .LBB0_2284
	s_lshl_b32 s3, s89, 3
	s_add_i32 s6, s3, s88
	s_cmpk_gt_i32 s6, 0x43ff
	s_mov_b32 s4, 6
	s_cbranch_scc1 .LBB0_2234
	s_ashr_i32 s5, s4, 31
	s_lshl_b32 s8, s34, 3
	s_lshl_b64 s[4:5], s[4:5], 3
	s_add_u32 s4, s0, s4
	s_addc_u32 s5, s1, s5
	s_load_dwordx2 s[4:5], s[4:5], 0x0
	s_waitcnt vmcnt(0)
	v_lshlrev_b32_e32 v18, 2, v250
	v_ashrrev_i32_e32 v19, 31, v18
	v_lshlrev_b64 v[20:21], 2, v[18:19]
	v_mbcnt_lo_u32_b32 v1, -1, 0
	s_waitcnt lgkmcnt(0)
	v_lshl_add_u64 v[2:3], s[4:5], 0, v[20:21]
	s_mov_b64 s[4:5], 0x3000
	v_lshl_add_u64 v[22:23], v[2:3], 0, s[4:5]
	v_add_co_u32_e32 v24, vcc, 0x3000, v2
	v_lshl_add_u64 v[20:21], s[26:27], 0, v[20:21]
	s_nop 0
	v_addc_co_u32_e32 v25, vcc, 0, v3, vcc
	global_load_dwordx4 v[2:5], v[22:23], off offset:1024
	global_load_dwordx4 v[6:9], v[22:23], off offset:2048
	global_load_dwordx4 v[10:13], v[24:25], off
	global_load_dwordx4 v[14:17], v[22:23], off offset:3072
	v_mbcnt_hi_u32_b32 v22, -1, v1
	v_and_b32_e32 v23, 64, v22
	v_xor_b32_e32 v1, 16, v22
	v_add_u32_e32 v23, 64, v23
	v_cmp_lt_i32_e32 vcc, v1, v23
	v_xor_b32_e32 v24, 32, v22
	s_mov_b64 s[4:5], 0x15a000
	v_cndmask_b32_e32 v1, v22, v1, vcc
	v_cmp_lt_i32_e32 vcc, v24, v23
	s_ashr_i32 s7, s6, 31
	s_mov_b32 s14, 0xdcbffa00
	v_cndmask_b32_e32 v22, v22, v24, vcc
	v_lshlrev_b32_e32 v94, 2, v22
	v_lshl_add_u64 v[22:23], v[20:21], 0, s[4:5]
	s_mov_b64 s[4:5], 0x15b000
	v_lshl_add_u64 v[24:25], v[20:21], 0, s[4:5]
	s_mov_b64 s[4:5], 0x159000
	v_lshl_add_u64 v[26:27], v[20:21], 0, s[4:5]
	s_lshl_b64 s[4:5], s[6:7], 11
	s_add_u32 s4, s26, s4
	s_addc_u32 s5, s27, s5
	v_lshl_add_u64 v[18:19], v[18:19], 1, s[4:5]
	s_mov_b64 s[4:5], 0x3eb00600
	s_ashr_i32 s9, s8, 31
	s_mov_b32 s16, 0xdcbffc00
	s_mov_b32 s18, 0xdcbffe00
	s_mov_b32 s20, 0xdcc00000
	s_mov_b32 s11, 0
	v_lshlrev_b32_e32 v1, 2, v1
	v_lshl_add_u64 v[28:29], v[18:19], 0, s[4:5]
	s_lshl_b64 s[12:13], s[8:9], 11
	s_mov_b32 s15, -1
	s_mov_b32 s3, 0xffff0000
	s_mov_b32 s17, -1
	s_mov_b32 s19, -1
	s_mov_b32 s21, -1
	s_mov_b32 s7, 0xfee00000
	s_mov_b32 s9, 0xff000000
	s_mov_b32 s22, 0xff200000
	s_mov_b32 s23, 0xff400000
	s_mov_b32 s30, 0xff600000
	s_mov_b32 s31, 0xff800000
	s_mov_b32 s33, 0xffa00000
	s_mov_b32 s36, 0xffc00000
	s_mov_b32 s37, 0xffe00000
	s_movk_i32 s40, 0x7fff
	v_mov_b32_e32 v95, 0x358637bd
	s_mov_b32 s41, 0xf800000
	v_mov_b32_e32 v96, 0x260
	s_mov_b32 s42, 0xe1000000
	v_mov_b32_e32 v97, 1
	v_add_co_u32_e32 v126, vcc, 0xdcc00000, v28
	s_nop 1
	v_addc_co_u32_e32 v127, vcc, -1, v29, vcc
	global_load_dwordx2 v[128:129], v[126:127], off offset:-1536
	global_load_dwordx2 v[130:131], v[126:127], off offset:-1024
	global_load_dwordx2 v[132:133], v[126:127], off offset:-512
	global_load_dwordx2 v[134:135], v[126:127], off
	s_waitcnt vmcnt(0)
	s_branch .LBB0_2232
.LBB0_2231:
	v_pk_mul_f32 v[62:63], v[32:33], v[32:33]
	v_pk_mul_f32 v[64:65], v[30:31], v[30:31]
	v_pk_mul_f32 v[58:59], v[34:35], v[34:35]
	v_pk_mul_f32 v[60:61], v[38:39], v[38:39]
	v_pk_mov_b32 v[66:67], v[64:65], v[62:63] op_sel:[1,0]
	v_mov_b32_e32 v65, v63
	v_pk_add_f32 v[62:63], v[66:67], v[64:65]
	v_pk_mov_b32 v[64:65], v[60:61], v[58:59] op_sel:[1,0]
	v_mov_b32_e32 v61, v59
	v_pk_add_f32 v[58:59], v[64:65], v[60:61]
	s_add_i32 s10, s6, 0xfffffc00
	v_pk_add_f32 v[58:59], v[58:59], v[58:59] op_sel_hi:[0,1]
	v_mul_f32_e32 v58, v44, v44
	s_lshr_b32 s10, s10, 12
	v_pk_fma_f32 v[60:61], v[44:45], v[44:45], v[58:59] op_sel_hi:[1,1,0]
	v_mul_f32_e32 v58, v40, v40
	s_mulk_i32 s10, 0x1800
	s_and_b64 s[4:5], s[4:5], exec
	v_pk_add_f32 v[62:63], v[62:63], v[62:63] op_sel_hi:[0,1]
	v_pk_fma_f32 v[64:65], v[40:41], v[40:41], v[58:59] op_sel_hi:[1,1,0]
	s_cselect_b32 s10, 0x6000, s10
	v_mul_f32_e32 v60, v36, v36
	v_mul_f32_e32 v64, v37, v37
	v_mul_f32_e32 v62, v42, v42
	v_mul_f32_e32 v58, v43, v43
	s_lshl_b64 s[4:5], s[10:11], 2
	v_pk_add_f32 v[66:67], v[60:61], v[64:65]
	v_pk_add_f32 v[68:69], v[62:63], v[58:59]
	v_lshl_add_u64 v[54:55], v[24:25], 0, s[4:5]
	v_lshl_add_u64 v[70:71], v[22:23], 0, s[4:5]
	v_pk_add_f32 v[66:67], v[66:67], v[68:69]
	global_load_dwordx4 v[18:21], v[54:55], off
	global_load_dwordx4 v[46:49], v[54:55], off offset:1024
	global_load_dwordx4 v[50:53], v[54:55], off offset:2048
	s_nop 0
	global_load_dwordx4 v[54:57], v[54:55], off offset:3072
	s_nop 0
	global_load_dwordx4 v[58:61], v[70:71], off offset:2048
	global_load_dwordx4 v[62:65], v[70:71], off offset:3072
	v_add_f32_e32 v74, v66, v67
	global_load_dwordx4 v[66:69], v[70:71], off
	s_nop 0
	global_load_dwordx4 v[70:73], v[70:71], off offset:1024
	v_lshl_add_u64 v[126:127], v[126:127], 0, s[12:13]
	global_load_dwordx2 v[128:129], v[126:127], off offset:-1536
	global_load_dwordx2 v[130:131], v[126:127], off offset:-1024
	global_load_dwordx2 v[132:133], v[126:127], off offset:-512
	global_load_dwordx2 v[134:135], v[126:127], off
	v_add_f32_dpp v74, v74, v74 row_ror:8 row_mask:0xf bank_mask:0xf bound_ctrl:1
	s_add_i32 s6, s6, s8
	s_cmpk_lt_i32 s6, 0x4400
	v_add_f32_dpp v74, v74, v74 row_ror:4 row_mask:0xf bank_mask:0xf bound_ctrl:1
	s_waitcnt vmcnt(11)
	v_pk_add_f32 v[18:19], v[18:19], 1.0 op_sel_hi:[1,0]
	v_add_f32_dpp v74, v74, v74 row_ror:2 row_mask:0xf bank_mask:0xf bound_ctrl:1
	v_pk_add_f32 v[20:21], v[20:21], 1.0 op_sel_hi:[1,0]
	s_waitcnt vmcnt(10)
	v_pk_add_f32 v[46:47], v[46:47], 1.0 op_sel_hi:[1,0]
	v_add_f32_dpp v74, v74, v74 row_ror:1 row_mask:0xf bank_mask:0xf bound_ctrl:1
	v_mov_b32_e32 v75, v74
	s_nop 1
	v_permlane16_swap_b32_e32 v74, v75
	v_pk_add_f32 v[48:49], v[48:49], 1.0 op_sel_hi:[1,0]
	s_waitcnt vmcnt(9)
	v_pk_add_f32 v[50:51], v[50:51], 1.0 op_sel_hi:[1,0]
	v_pk_add_f32 v[52:53], v[52:53], 1.0 op_sel_hi:[1,0]
	s_waitcnt vmcnt(8)
	v_pk_add_f32 v[54:55], v[54:55], 1.0 op_sel_hi:[1,0]
	s_waitcnt lgkmcnt(0)
	v_add_f32_e32 v74, v74, v75
	v_mov_b32_e32 v75, v74
	s_nop 1
	v_permlane32_swap_b32_e32 v74, v75
	v_pk_add_f32 v[56:57], v[56:57], 1.0 op_sel_hi:[1,0]
	s_waitcnt lgkmcnt(0)
	v_add_f32_e32 v74, v74, v75
	v_fmamk_f32 v74, v74, 0x3a800000, v95
	v_mul_f32_e32 v75, 0x4f800000, v74
	v_cmp_gt_f32_e32 vcc, s41, v74
	s_nop 1
	v_cndmask_b32_e32 v74, v74, v75, vcc
	v_sqrt_f32_e32 v75, v74
	s_nop 0
	v_add_u32_e32 v76, -1, v75
	v_add_u32_e32 v77, 1, v75
	v_fma_f32 v78, -v76, v75, v74
	v_fma_f32 v79, -v77, v75, v74
	v_cmp_ge_f32_e64 s[4:5], 0, v78
	s_nop 1
	v_cndmask_b32_e64 v75, v75, v76, s[4:5]
	v_cmp_lt_f32_e64 s[4:5], 0, v79
	s_nop 1
	v_cndmask_b32_e64 v75, v75, v77, s[4:5]
	v_mul_f32_e32 v76, 0x37800000, v75
	v_cndmask_b32_e32 v75, v75, v76, vcc
	v_cmp_class_f32_e32 vcc, v74, v96
	s_nop 1
	v_cndmask_b32_e32 v74, v75, v74, vcc
	v_div_scale_f32 v75, s[4:5], v74, v74, 1.0
	v_rcp_f32_e32 v76, v75
	v_div_scale_f32 v77, vcc, 1.0, v74, 1.0
	v_fma_f32 v78, -v75, v76, 1.0
	v_fmac_f32_e32 v76, v78, v76
	v_mul_f32_e32 v78, v77, v76
	v_fma_f32 v79, -v75, v78, v77
	v_fmac_f32_e32 v78, v79, v76
	v_fma_f32 v75, -v75, v78, v77
	v_div_fmas_f32 v75, v75, v76, v78
	v_div_fixup_f32 v74, v75, v74, 1.0
	v_pk_mul_f32 v[30:31], v[30:31], v[74:75] op_sel_hi:[1,0]
	v_pk_mul_f32 v[32:33], v[32:33], v[74:75] op_sel_hi:[1,0]
	v_pk_mul_f32 v[30:31], v[10:11], v[30:31]
	v_pk_mul_f32 v[32:33], v[12:13], v[32:33]
	s_waitcnt vmcnt(5)
	v_pk_fma_f32 v[18:19], v[18:19], v[30:31], v[66:67]
	v_pk_fma_f32 v[20:21], v[20:21], v[32:33], v[68:69]
	v_bfe_u32 v30, v18, 16, 1
	v_add3_u32 v18, v18, v30, s40
	v_bfe_u32 v30, v19, 16, 1
	v_lshrrev_b32_e32 v18, 16, v18
	v_add3_u32 v19, v19, v30, s40
	v_and_or_b32 v18, v19, s3, v18
	v_bfe_u32 v19, v20, 16, 1
	v_add3_u32 v19, v20, v19, s40
	v_bfe_u32 v20, v21, 16, 1
	v_pk_mul_f32 v[38:39], v[38:39], v[74:75] op_sel_hi:[1,0]
	v_lshrrev_b32_e32 v19, 16, v19
	v_add3_u32 v20, v21, v20, s40
	v_pk_mul_f32 v[38:39], v[2:3], v[38:39]
	v_and_or_b32 v19, v20, s3, v19
	v_add_co_u32_e32 v20, vcc, s42, v28
	s_waitcnt vmcnt(4)
	v_pk_fma_f32 v[38:39], v[46:47], v[38:39], v[70:71]
	v_addc_co_u32_e32 v21, vcc, -1, v29, vcc
	v_pk_mul_f32 v[34:35], v[34:35], v[74:75] op_sel_hi:[1,0]
	global_store_dwordx2 v[20:21], v[18:19], off offset:-1536
	v_pk_mul_f32 v[34:35], v[4:5], v[34:35]
	v_pk_fma_f32 v[34:35], v[48:49], v[34:35], v[72:73]
	v_cvt_pk_bf16_f32 v18, v38, v39
	v_pk_mul_f32 v[44:45], v[44:45], v[74:75] op_sel_hi:[1,0]
	v_pk_mul_f32 v[44:45], v[6:7], v[44:45]
	v_pk_fma_f32 v[44:45], v[50:51], v[44:45], v[58:59]
	v_cvt_pk_bf16_f32 v19, v34, v35
	v_pk_mul_f32 v[40:41], v[40:41], v[74:75] op_sel_hi:[1,0]
	global_store_dwordx2 v[20:21], v[18:19], off offset:-1024
	v_pk_mul_f32 v[40:41], v[8:9], v[40:41]
	v_pk_fma_f32 v[40:41], v[52:53], v[40:41], v[60:61]
	v_cvt_pk_bf16_f32 v18, v44, v45
	v_pk_mul_f32 v[36:37], v[36:37], v[74:75] op_sel_hi:[1,0]
	v_pk_mul_f32 v[36:37], v[14:15], v[36:37]
	v_pk_fma_f32 v[36:37], v[54:55], v[36:37], v[62:63]
	v_cvt_pk_bf16_f32 v19, v40, v41
	v_pk_mul_f32 v[42:43], v[42:43], v[74:75] op_sel_hi:[1,0]
	global_store_dwordx2 v[20:21], v[18:19], off offset:-512
	v_pk_mul_f32 v[42:43], v[16:17], v[42:43]
	v_pk_fma_f32 v[42:43], v[56:57], v[42:43], v[64:65]
	v_cvt_pk_bf16_f32 v18, v36, v37
	v_cvt_pk_bf16_f32 v19, v42, v43
	v_lshl_add_u64 v[28:29], v[28:29], 0, s[12:13]
	global_store_dwordx2 v[20:21], v[18:19], off
	s_cbranch_scc0 .LBB0_2234
.LBB0_2232:
	s_waitcnt vmcnt(4)
	s_cmpk_lt_i32 s6, 0x400
	s_cselect_b64 s[4:5], -1, 0
	s_cmpk_gt_i32 s6, 0x3ff
	v_lshlrev_b32_e32 v30, 16, v128
	v_and_b32_e32 v31, 0xffff0000, v128
	v_lshlrev_b32_e32 v32, 16, v129
	v_and_b32_e32 v33, 0xffff0000, v129
	v_lshlrev_b32_e32 v38, 16, v130
	v_and_b32_e32 v39, 0xffff0000, v130
	v_lshlrev_b32_e32 v34, 16, v131
	v_and_b32_e32 v35, 0xffff0000, v131
	v_lshlrev_b32_e32 v44, 16, v132
	v_and_b32_e32 v45, 0xffff0000, v132
	v_lshlrev_b32_e32 v40, 16, v133
	v_and_b32_e32 v41, 0xffff0000, v133
	v_lshlrev_b32_e32 v36, 16, v134
	v_and_b32_e32 v37, 0xffff0000, v134
	v_lshlrev_b32_e32 v42, 16, v135
	v_and_b32_e32 v43, 0xffff0000, v135
	s_cbranch_scc1 .LBB0_2231
	v_add_co_u32_e32 v76, vcc, 0xfec00000, v28
	v_lshl_add_u64 v[46:47], v[28:29], 0, s[14:15]
	s_nop 0
	v_addc_co_u32_e32 v77, vcc, -1, v29, vcc
	v_add_co_u32_e32 v74, vcc, s7, v28
	global_load_dwordx2 v[50:51], v[76:77], off offset:-1536
	s_nop 0
	v_addc_co_u32_e32 v75, vcc, -1, v29, vcc
	v_add_co_u32_e32 v78, vcc, s9, v28
	global_load_dwordx2 v[48:49], v[28:29], off offset:-1536
	s_nop 0
	v_addc_co_u32_e32 v79, vcc, -1, v29, vcc
	v_add_co_u32_e32 v66, vcc, s22, v28
	global_load_dwordx2 v[72:73], v[78:79], off offset:-1536
	global_load_dwordx2 v[52:53], v[74:75], off offset:-1536
	v_addc_co_u32_e32 v67, vcc, -1, v29, vcc
	v_add_co_u32_e32 v62, vcc, s23, v28
	global_load_dwordx2 v[70:71], v[66:67], off offset:-1536
	s_nop 0
	v_addc_co_u32_e32 v63, vcc, -1, v29, vcc
	v_add_co_u32_e32 v56, vcc, s30, v28
	global_load_dwordx2 v[68:69], v[62:63], off offset:-1536
	s_nop 0
	v_addc_co_u32_e32 v57, vcc, -1, v29, vcc
	v_add_co_u32_e32 v54, vcc, s31, v28
	global_load_dwordx2 v[64:65], v[56:57], off offset:-1536
	s_nop 0
	v_addc_co_u32_e32 v55, vcc, -1, v29, vcc
	global_load_dwordx2 v[58:59], v[54:55], off offset:-1536
	v_add_co_u32_e32 v84, vcc, s33, v28
	s_waitcnt vmcnt(7)
	v_lshlrev_b32_e32 v106, 16, v50
	v_addc_co_u32_e32 v85, vcc, -1, v29, vcc
	global_load_dwordx2 v[86:87], v[84:85], off offset:-1536
	global_load_dwordx4 v[18:21], v[26:27], off
	v_add_co_u32_e32 v80, vcc, s36, v28
	v_and_b32_e32 v107, 0xffff0000, v50
	s_nop 0
	v_addc_co_u32_e32 v81, vcc, -1, v29, vcc
	global_load_dwordx2 v[82:83], v[80:81], off offset:-1536
	global_load_dwordx2 v[60:61], v[76:77], off offset:-1024
	global_load_dwordx2 v[88:89], v[76:77], off offset:-512
	s_nop 0
	global_load_dwordx2 v[76:77], v[76:77], off
	v_add_co_u32_e32 v98, vcc, s37, v28
	v_lshlrev_b32_e32 v50, 16, v51
	s_nop 0
	v_addc_co_u32_e32 v99, vcc, -1, v29, vcc
	global_load_dwordx2 v[100:101], v[98:99], off offset:-1536
	global_load_dwordx2 v[102:103], v[74:75], off offset:-1024
	global_load_dwordx2 v[90:91], v[74:75], off offset:-512
	s_nop 0
	global_load_dwordx2 v[74:75], v[74:75], off
	s_nop 0
	global_load_dwordx2 v[104:105], v[78:79], off offset:-1024
	global_load_dwordx2 v[92:93], v[78:79], off offset:-512
	s_nop 0
	global_load_dwordx2 v[78:79], v[78:79], off
	v_and_b32_e32 v51, 0xffff0000, v51
	v_pk_add_f32 v[50:51], v[50:51], 0 op_sel_hi:[1,0]
	v_pk_add_f32 v[106:107], v[106:107], 0 op_sel_hi:[1,0]
	s_waitcnt vmcnt(17)
	v_lshlrev_b32_e32 v108, 16, v52
	v_and_b32_e32 v109, 0xffff0000, v52
	v_lshlrev_b32_e32 v52, 16, v53
	v_and_b32_e32 v53, 0xffff0000, v53
	v_pk_add_f32 v[106:107], v[106:107], v[108:109]
	v_pk_add_f32 v[50:51], v[50:51], v[52:53]
	v_lshlrev_b32_e32 v52, 16, v72
	v_and_b32_e32 v53, 0xffff0000, v72
	v_lshlrev_b32_e32 v72, 16, v73
	v_and_b32_e32 v73, 0xffff0000, v73
	v_pk_add_f32 v[108:109], v[50:51], v[72:73]
	v_pk_add_f32 v[52:53], v[106:107], v[52:53]
	global_load_dwordx2 v[106:107], v[66:67], off offset:-1024
	global_load_dwordx2 v[72:73], v[66:67], off offset:-512
	global_load_dwordx2 v[50:51], v[66:67], off
	s_waitcnt vmcnt(19)
	v_lshlrev_b32_e32 v66, 16, v70
	v_and_b32_e32 v67, 0xffff0000, v70
	v_lshlrev_b32_e32 v70, 16, v71
	v_and_b32_e32 v71, 0xffff0000, v71
	v_pk_add_f32 v[66:67], v[52:53], v[66:67]
	v_pk_add_f32 v[108:109], v[108:109], v[70:71]
	global_load_dwordx2 v[110:111], v[62:63], off offset:-1024
	global_load_dwordx2 v[70:71], v[62:63], off offset:-512
	global_load_dwordx2 v[52:53], v[62:63], off
	s_waitcnt vmcnt(21)
	v_lshlrev_b32_e32 v62, 16, v68
	v_and_b32_e32 v63, 0xffff0000, v68
	v_lshlrev_b32_e32 v68, 16, v69
	v_and_b32_e32 v69, 0xffff0000, v69
	v_pk_add_f32 v[108:109], v[108:109], v[68:69]
	v_pk_add_f32 v[62:63], v[66:67], v[62:63]
	s_waitcnt vmcnt(20)
	v_lshlrev_b32_e32 v66, 16, v64
	v_and_b32_e32 v67, 0xffff0000, v64
	v_lshlrev_b32_e32 v64, 16, v65
	v_and_b32_e32 v65, 0xffff0000, v65
	v_pk_add_f32 v[62:63], v[62:63], v[66:67]
	v_pk_add_f32 v[64:65], v[108:109], v[64:65]
	s_waitcnt vmcnt(19)
	v_lshlrev_b32_e32 v66, 16, v58
	v_and_b32_e32 v67, 0xffff0000, v58
	v_lshlrev_b32_e32 v58, 16, v59
	v_and_b32_e32 v59, 0xffff0000, v59
	global_load_dwordx2 v[112:113], v[56:57], off offset:-1024
	global_load_dwordx2 v[68:69], v[56:57], off offset:-512
	s_nop 0
	global_load_dwordx2 v[56:57], v[56:57], off
	s_nop 0
	global_load_dwordx2 v[108:109], v[54:55], off offset:-1024
	global_load_dwordx2 v[114:115], v[54:55], off offset:-512
	s_nop 0
	global_load_dwordx2 v[54:55], v[54:55], off
	v_pk_add_f32 v[64:65], v[64:65], v[58:59]
	v_pk_add_f32 v[62:63], v[62:63], v[66:67]
	global_load_dwordx2 v[116:117], v[84:85], off offset:-1024
	global_load_dwordx2 v[118:119], v[84:85], off offset:-512
	global_load_dwordx2 v[58:59], v[84:85], off
	v_lshlrev_b32_e32 v124, 16, v48
	v_and_b32_e32 v125, 0xffff0000, v48
	v_lshlrev_b32_e32 v48, 16, v49
	v_and_b32_e32 v49, 0xffff0000, v49
	s_waitcnt vmcnt(27)
	v_lshlrev_b32_e32 v66, 16, v86
	v_and_b32_e32 v67, 0xffff0000, v86
	v_lshlrev_b32_e32 v84, 16, v87
	v_and_b32_e32 v85, 0xffff0000, v87
	v_pk_add_f32 v[66:67], v[62:63], v[66:67]
	v_pk_add_f32 v[64:65], v[64:65], v[84:85]
	global_load_dwordx2 v[84:85], v[80:81], off offset:-1024
	global_load_dwordx2 v[86:87], v[80:81], off offset:-512
	global_load_dwordx2 v[62:63], v[80:81], off
	s_waitcnt vmcnt(28)
	v_lshlrev_b32_e32 v80, 16, v82
	v_and_b32_e32 v81, 0xffff0000, v82
	v_lshlrev_b32_e32 v82, 16, v83
	v_and_b32_e32 v83, 0xffff0000, v83
	v_pk_add_f32 v[82:83], v[64:65], v[82:83]
	v_pk_add_f32 v[66:67], v[66:67], v[80:81]
	global_load_dwordx2 v[80:81], v[98:99], off offset:-1024
	global_load_dwordx2 v[120:121], v[98:99], off offset:-512
	global_load_dwordx2 v[64:65], v[98:99], off
	s_waitcnt vmcnt(27)
	v_lshlrev_b32_e32 v98, 16, v100
	v_and_b32_e32 v99, 0xffff0000, v100
	v_lshlrev_b32_e32 v100, 16, v101
	v_and_b32_e32 v101, 0xffff0000, v101
	v_pk_add_f32 v[98:99], v[66:67], v[98:99]
	v_pk_add_f32 v[82:83], v[82:83], v[100:101]
	global_load_dwordx2 v[100:101], v[28:29], off offset:-1024
	global_load_dwordx2 v[122:123], v[28:29], off offset:-512
	global_load_dwordx2 v[66:67], v[28:29], off
	v_pk_add_f32 v[48:49], v[82:83], v[48:49]
	v_pk_add_f32 v[82:83], v[98:99], v[124:125]
	v_pk_fma_f32 v[32:33], v[48:49], v[20:21], v[32:33]
	v_pk_fma_f32 v[18:19], v[82:83], v[18:19], v[30:31]
	v_lshlrev_b32_e32 v48, 16, v60
	v_bfe_u32 v20, v18, 16, 1
	v_add3_u32 v30, v18, v20, s40
	v_bfe_u32 v18, v19, 16, 1
	v_and_b32_sdwa v20, v33, v97 dst_sel:DWORD dst_unused:UNUSED_PAD src0_sel:WORD_1 src1_sel:DWORD
	v_add3_u32 v18, v19, v18, s40
	v_bfe_u32 v19, v32, 16, 1
	v_add3_u32 v20, v33, v20, s40
	v_and_b32_e32 v31, 0xffff0000, v18
	v_add3_u32 v19, v32, v19, s40
	v_and_b32_e32 v33, 0xffff0000, v20
	v_or_b32_sdwa v18, v31, v30 dst_sel:DWORD dst_unused:UNUSED_PAD src0_sel:DWORD src1_sel:WORD_1
	v_or_b32_sdwa v19, v33, v19 dst_sel:DWORD dst_unused:UNUSED_PAD src0_sel:DWORD src1_sel:WORD_1
	global_store_dwordx2 v[46:47], v[18:19], off
	global_load_dwordx4 v[18:21], v[26:27], off offset:1024
	v_and_b32_e32 v49, 0xffff0000, v60
	v_lshlrev_b32_e32 v60, 16, v61
	v_and_b32_e32 v61, 0xffff0000, v61
	v_pk_add_f32 v[48:49], v[48:49], 0 op_sel_hi:[1,0]
	v_pk_add_f32 v[60:61], v[60:61], 0 op_sel_hi:[1,0]
	s_waitcnt vmcnt(31)
	v_lshlrev_b32_e32 v82, 16, v102
	v_and_b32_e32 v83, 0xffff0000, v102
	v_lshlrev_b32_e32 v98, 16, v103
	v_and_b32_e32 v99, 0xffff0000, v103
	v_pk_add_f32 v[60:61], v[60:61], v[98:99]
	v_pk_add_f32 v[48:49], v[48:49], v[82:83]
	s_waitcnt vmcnt(28)
	v_lshlrev_b32_e32 v82, 16, v104
	v_and_b32_e32 v83, 0xffff0000, v104
	v_lshlrev_b32_e32 v98, 16, v105
	v_and_b32_e32 v99, 0xffff0000, v105
	v_pk_add_f32 v[48:49], v[48:49], v[82:83]
	v_pk_add_f32 v[60:61], v[60:61], v[98:99]
	s_waitcnt vmcnt(25)
	v_lshlrev_b32_e32 v82, 16, v106
	v_and_b32_e32 v83, 0xffff0000, v106
	v_lshlrev_b32_e32 v98, 16, v107
	v_and_b32_e32 v99, 0xffff0000, v107
	v_pk_add_f32 v[60:61], v[60:61], v[98:99]
	v_pk_add_f32 v[48:49], v[48:49], v[82:83]
	s_waitcnt vmcnt(22)
	v_lshlrev_b32_e32 v82, 16, v110
	v_and_b32_e32 v83, 0xffff0000, v110
	v_lshlrev_b32_e32 v98, 16, v111
	v_and_b32_e32 v99, 0xffff0000, v111
	v_pk_add_f32 v[48:49], v[48:49], v[82:83]
	v_pk_add_f32 v[60:61], v[60:61], v[98:99]
	s_waitcnt vmcnt(19)
	v_lshlrev_b32_e32 v82, 16, v112
	v_and_b32_e32 v83, 0xffff0000, v112
	v_lshlrev_b32_e32 v98, 16, v113
	v_and_b32_e32 v99, 0xffff0000, v113
	v_pk_add_f32 v[60:61], v[60:61], v[98:99]
	v_pk_add_f32 v[48:49], v[48:49], v[82:83]
	s_waitcnt vmcnt(16)
	v_lshlrev_b32_e32 v82, 16, v108
	v_and_b32_e32 v83, 0xffff0000, v108
	v_lshlrev_b32_e32 v98, 16, v109
	v_and_b32_e32 v99, 0xffff0000, v109
	v_pk_add_f32 v[48:49], v[48:49], v[82:83]
	v_pk_add_f32 v[60:61], v[60:61], v[98:99]
	s_waitcnt vmcnt(13)
	v_lshlrev_b32_e32 v82, 16, v116
	v_and_b32_e32 v83, 0xffff0000, v116
	v_lshlrev_b32_e32 v98, 16, v117
	v_and_b32_e32 v99, 0xffff0000, v117
	v_pk_add_f32 v[60:61], v[60:61], v[98:99]
	v_pk_add_f32 v[48:49], v[48:49], v[82:83]
	s_waitcnt vmcnt(10)
	v_lshlrev_b32_e32 v82, 16, v84
	v_and_b32_e32 v83, 0xffff0000, v84
	v_lshlrev_b32_e32 v84, 16, v85
	v_and_b32_e32 v85, 0xffff0000, v85
	v_pk_add_f32 v[48:49], v[48:49], v[82:83]
	v_pk_add_f32 v[60:61], v[60:61], v[84:85]
	s_waitcnt vmcnt(7)
	v_lshlrev_b32_e32 v82, 16, v80
	v_and_b32_e32 v83, 0xffff0000, v80
	v_lshlrev_b32_e32 v80, 16, v81
	v_and_b32_e32 v81, 0xffff0000, v81
	v_pk_add_f32 v[60:61], v[60:61], v[80:81]
	v_pk_add_f32 v[48:49], v[48:49], v[82:83]
	s_waitcnt vmcnt(4)
	v_lshlrev_b32_e32 v80, 16, v100
	v_and_b32_e32 v81, 0xffff0000, v100
	v_pk_add_f32 v[48:49], v[48:49], v[80:81]
	v_lshlrev_b32_e32 v82, 16, v101
	v_and_b32_e32 v83, 0xffff0000, v101
	v_pk_add_f32 v[60:61], v[60:61], v[82:83]
	v_lshl_add_u64 v[46:47], v[28:29], 0, s[16:17]
	v_lshlrev_b32_e32 v80, 16, v89
	v_and_b32_e32 v81, 0xffff0000, v89
	v_pk_add_f32 v[80:81], v[80:81], 0 op_sel_hi:[1,0]
	v_lshlrev_b32_e32 v82, 16, v90
	v_and_b32_e32 v83, 0xffff0000, v90
	v_lshlrev_b32_e32 v84, 16, v91
	v_and_b32_e32 v85, 0xffff0000, v91
	v_pk_add_f32 v[80:81], v[80:81], v[84:85]
	v_lshlrev_b32_e32 v84, 16, v93
	v_and_b32_e32 v85, 0xffff0000, v93
	v_pk_add_f32 v[80:81], v[80:81], v[84:85]
	v_and_b32_e32 v30, 0xffff0000, v30
	s_waitcnt vmcnt(0)
	v_pk_fma_f32 v[38:39], v[48:49], v[18:19], v[38:39]
	s_nop 0
	v_pk_fma_f32 v[34:35], v[60:61], v[20:21], v[34:35]
	v_and_b32_sdwa v20, v35, v97 dst_sel:DWORD dst_unused:UNUSED_PAD src0_sel:WORD_1 src1_sel:DWORD
	v_cvt_pk_bf16_f32 v18, v38, v39
	v_bfe_u32 v19, v34, 16, 1
	v_add3_u32 v20, v35, v20, s40
	v_add3_u32 v19, v34, v19, s40
	v_and_b32_e32 v35, 0xffff0000, v20
	v_or_b32_sdwa v19, v35, v19 dst_sel:DWORD dst_unused:UNUSED_PAD src0_sel:DWORD src1_sel:WORD_1
	global_store_dwordx2 v[46:47], v[18:19], off
	global_load_dwordx4 v[18:21], v[26:27], off offset:2048
	v_and_b32_sdwa v60, v32, v97 dst_sel:DWORD dst_unused:UNUSED_PAD src0_sel:WORD_1 src1_sel:DWORD
	v_add3_u32 v32, v32, v60, s40
	v_and_b32_sdwa v60, v39, v97 dst_sel:DWORD dst_unused:UNUSED_PAD src0_sel:WORD_1 src1_sel:DWORD
	v_and_b32_sdwa v61, v38, v97 dst_sel:DWORD dst_unused:UNUSED_PAD src0_sel:WORD_1 src1_sel:DWORD
	v_add3_u32 v39, v39, v60, s40
	v_add3_u32 v38, v38, v61, s40
	v_lshlrev_b32_e32 v60, 16, v88
	v_and_b32_e32 v61, 0xffff0000, v88
	v_pk_add_f32 v[60:61], v[60:61], 0 op_sel_hi:[1,0]
	v_lshl_add_u64 v[46:47], v[28:29], 0, s[18:19]
	v_pk_add_f32 v[60:61], v[60:61], v[82:83]
	v_lshlrev_b32_e32 v82, 16, v92
	v_and_b32_e32 v83, 0xffff0000, v92
	v_pk_add_f32 v[60:61], v[60:61], v[82:83]
	v_lshlrev_b32_e32 v82, 16, v72
	v_and_b32_e32 v83, 0xffff0000, v72
	v_lshlrev_b32_e32 v72, 16, v73
	v_and_b32_e32 v73, 0xffff0000, v73
	v_pk_add_f32 v[72:73], v[80:81], v[72:73]
	v_pk_add_f32 v[60:61], v[60:61], v[82:83]
	v_lshlrev_b32_e32 v80, 16, v70
	v_and_b32_e32 v81, 0xffff0000, v70
	v_lshlrev_b32_e32 v70, 16, v71
	v_and_b32_e32 v71, 0xffff0000, v71
	v_pk_add_f32 v[60:61], v[60:61], v[80:81]
	v_pk_add_f32 v[70:71], v[72:73], v[70:71]
	v_lshlrev_b32_e32 v72, 16, v68
	v_and_b32_e32 v73, 0xffff0000, v68
	v_lshlrev_b32_e32 v68, 16, v69
	v_and_b32_e32 v69, 0xffff0000, v69
	v_pk_add_f32 v[68:69], v[70:71], v[68:69]
	v_pk_add_f32 v[60:61], v[60:61], v[72:73]
	v_lshlrev_b32_e32 v70, 16, v114
	v_and_b32_e32 v71, 0xffff0000, v114
	v_pk_add_f32 v[60:61], v[60:61], v[70:71]
	v_lshlrev_b32_e32 v70, 16, v118
	v_and_b32_e32 v71, 0xffff0000, v118
	v_lshlrev_b32_e32 v72, 16, v115
	v_and_b32_e32 v73, 0xffff0000, v115
	v_pk_add_f32 v[60:61], v[60:61], v[70:71]
	v_lshlrev_b32_e32 v70, 16, v86
	v_and_b32_e32 v71, 0xffff0000, v86
	v_pk_add_f32 v[68:69], v[68:69], v[72:73]
	v_lshlrev_b32_e32 v72, 16, v119
	v_and_b32_e32 v73, 0xffff0000, v119
	v_pk_add_f32 v[60:61], v[60:61], v[70:71]
	v_lshlrev_b32_e32 v70, 16, v120
	v_and_b32_e32 v71, 0xffff0000, v120
	v_pk_add_f32 v[68:69], v[68:69], v[72:73]
	v_lshlrev_b32_e32 v72, 16, v87
	v_and_b32_e32 v73, 0xffff0000, v87
	v_pk_add_f32 v[60:61], v[60:61], v[70:71]
	v_lshlrev_b32_e32 v70, 16, v122
	v_and_b32_e32 v71, 0xffff0000, v122
	v_pk_add_f32 v[68:69], v[68:69], v[72:73]
	v_lshlrev_b32_e32 v72, 16, v121
	v_and_b32_e32 v73, 0xffff0000, v121
	v_pk_add_f32 v[60:61], v[60:61], v[70:71]
	v_pk_add_f32 v[68:69], v[68:69], v[72:73]
	v_lshlrev_b32_e32 v72, 16, v123
	v_and_b32_e32 v73, 0xffff0000, v123
	v_pk_add_f32 v[68:69], v[68:69], v[72:73]
	v_lshlrev_b32_e32 v70, 16, v75
	v_and_b32_e32 v71, 0xffff0000, v75
	v_lshl_add_u64 v[48:49], v[28:29], 0, s[20:21]
	v_and_b32_e32 v32, 0xffff0000, v32
	v_and_b32_e32 v39, 0xffff0000, v39
	v_and_b32_e32 v38, 0xffff0000, v38
	s_waitcnt vmcnt(0)
	v_pk_fma_f32 v[44:45], v[60:61], v[18:19], v[44:45]
	s_nop 0
	v_pk_fma_f32 v[40:41], v[68:69], v[20:21], v[40:41]
	v_and_b32_sdwa v20, v41, v97 dst_sel:DWORD dst_unused:UNUSED_PAD src0_sel:WORD_1 src1_sel:DWORD
	v_cvt_pk_bf16_f32 v18, v44, v45
	v_bfe_u32 v19, v40, 16, 1
	v_add3_u32 v20, v41, v20, s40
	v_add3_u32 v19, v40, v19, s40
	v_and_b32_e32 v41, 0xffff0000, v20
	v_or_b32_sdwa v19, v41, v19 dst_sel:DWORD dst_unused:UNUSED_PAD src0_sel:DWORD src1_sel:WORD_1
	global_store_dwordx2 v[46:47], v[18:19], off
	global_load_dwordx4 v[18:21], v[26:27], off offset:3072
	v_and_b32_sdwa v46, v34, v97 dst_sel:DWORD dst_unused:UNUSED_PAD src0_sel:WORD_1 src1_sel:DWORD
	v_add3_u32 v34, v34, v46, s40
	v_and_b32_sdwa v46, v45, v97 dst_sel:DWORD dst_unused:UNUSED_PAD src0_sel:WORD_1 src1_sel:DWORD
	v_and_b32_sdwa v47, v44, v97 dst_sel:DWORD dst_unused:UNUSED_PAD src0_sel:WORD_1 src1_sel:DWORD
	v_add3_u32 v45, v45, v46, s40
	v_add3_u32 v44, v44, v47, s40
	v_lshlrev_b32_e32 v46, 16, v76
	v_and_b32_e32 v47, 0xffff0000, v76
	v_lshlrev_b32_e32 v60, 16, v77
	v_and_b32_e32 v61, 0xffff0000, v77
	v_pk_add_f32 v[46:47], v[46:47], 0 op_sel_hi:[1,0]
	v_pk_add_f32 v[60:61], v[60:61], 0 op_sel_hi:[1,0]
	v_lshlrev_b32_e32 v68, 16, v74
	v_and_b32_e32 v69, 0xffff0000, v74
	v_pk_add_f32 v[60:61], v[60:61], v[70:71]
	v_pk_add_f32 v[46:47], v[46:47], v[68:69]
	v_lshlrev_b32_e32 v68, 16, v78
	v_and_b32_e32 v69, 0xffff0000, v78
	v_lshlrev_b32_e32 v70, 16, v79
	v_and_b32_e32 v71, 0xffff0000, v79
	v_pk_add_f32 v[46:47], v[46:47], v[68:69]
	v_pk_add_f32 v[60:61], v[60:61], v[70:71]
	v_lshlrev_b32_e32 v68, 16, v50
	v_and_b32_e32 v69, 0xffff0000, v50
	v_lshlrev_b32_e32 v50, 16, v51
	v_and_b32_e32 v51, 0xffff0000, v51
	v_pk_add_f32 v[50:51], v[60:61], v[50:51]
	v_pk_add_f32 v[46:47], v[46:47], v[68:69]
	v_lshlrev_b32_e32 v60, 16, v52
	v_and_b32_e32 v61, 0xffff0000, v52
	v_lshlrev_b32_e32 v52, 16, v53
	v_and_b32_e32 v53, 0xffff0000, v53
	v_pk_add_f32 v[46:47], v[46:47], v[60:61]
	v_pk_add_f32 v[50:51], v[50:51], v[52:53]
	v_lshlrev_b32_e32 v52, 16, v56
	v_and_b32_e32 v53, 0xffff0000, v56
	v_pk_add_f32 v[46:47], v[46:47], v[52:53]
	v_lshlrev_b32_e32 v52, 16, v54
	v_and_b32_e32 v53, 0xffff0000, v54
	v_pk_add_f32 v[46:47], v[46:47], v[52:53]
	v_lshlrev_b32_e32 v52, 16, v58
	v_and_b32_e32 v53, 0xffff0000, v58
	v_lshlrev_b32_e32 v56, 16, v57
	v_and_b32_e32 v57, 0xffff0000, v57
	v_pk_add_f32 v[46:47], v[46:47], v[52:53]
	v_lshlrev_b32_e32 v52, 16, v62
	v_and_b32_e32 v53, 0xffff0000, v62
	v_pk_add_f32 v[50:51], v[50:51], v[56:57]
	v_lshlrev_b32_e32 v54, 16, v55
	v_and_b32_e32 v55, 0xffff0000, v55
	v_pk_add_f32 v[46:47], v[46:47], v[52:53]
	v_lshlrev_b32_e32 v52, 16, v64
	v_and_b32_e32 v53, 0xffff0000, v64
	v_pk_add_f32 v[50:51], v[50:51], v[54:55]
	v_lshlrev_b32_e32 v54, 16, v59
	v_and_b32_e32 v55, 0xffff0000, v59
	v_pk_add_f32 v[46:47], v[46:47], v[52:53]
	v_lshlrev_b32_e32 v52, 16, v66
	v_and_b32_e32 v53, 0xffff0000, v66
	v_pk_add_f32 v[50:51], v[50:51], v[54:55]
	v_lshlrev_b32_e32 v54, 16, v63
	v_and_b32_e32 v55, 0xffff0000, v63
	v_pk_add_f32 v[46:47], v[46:47], v[52:53]
	v_pk_add_f32 v[50:51], v[50:51], v[54:55]
	v_lshlrev_b32_e32 v54, 16, v65
	v_and_b32_e32 v55, 0xffff0000, v65
	v_pk_add_f32 v[50:51], v[50:51], v[54:55]
	v_lshlrev_b32_e32 v54, 16, v67
	v_and_b32_e32 v55, 0xffff0000, v67
	v_pk_add_f32 v[50:51], v[50:51], v[54:55]
	v_and_b32_sdwa v52, v40, v97 dst_sel:DWORD dst_unused:UNUSED_PAD src0_sel:WORD_1 src1_sel:DWORD
	v_add3_u32 v40, v40, v52, s40
	v_and_b32_e32 v34, 0xffff0000, v34
	v_and_b32_e32 v45, 0xffff0000, v45
	v_and_b32_e32 v44, 0xffff0000, v44
	v_and_b32_e32 v40, 0xffff0000, v40
	s_waitcnt vmcnt(0)
	v_pk_fma_f32 v[18:19], v[46:47], v[18:19], v[36:37]
	s_nop 0
	v_pk_fma_f32 v[20:21], v[50:51], v[20:21], v[42:43]
	v_cvt_pk_bf16_f32 v46, v18, v19
	v_bfe_u32 v36, v20, 16, 1
	v_and_b32_sdwa v37, v18, v97 dst_sel:DWORD dst_unused:UNUSED_PAD src0_sel:WORD_1 src1_sel:DWORD
	v_add3_u32 v47, v20, v36, s40
	v_and_b32_sdwa v36, v19, v97 dst_sel:DWORD dst_unused:UNUSED_PAD src0_sel:WORD_1 src1_sel:DWORD
	v_add3_u32 v18, v18, v37, s40
	v_add3_u32 v19, v19, v36, s40
	v_and_b32_e32 v36, 0xffff0000, v18
	v_and_b32_sdwa v18, v21, v97 dst_sel:DWORD dst_unused:UNUSED_PAD src0_sel:WORD_1 src1_sel:DWORD
	v_and_b32_e32 v37, 0xffff0000, v19
	v_and_b32_sdwa v19, v20, v97 dst_sel:DWORD dst_unused:UNUSED_PAD src0_sel:WORD_1 src1_sel:DWORD
	v_add3_u32 v18, v21, v18, s40
	v_add3_u32 v19, v20, v19, s40
	v_and_b32_e32 v43, 0xffff0000, v18
	v_and_b32_e32 v42, 0xffff0000, v19
	v_or_b32_sdwa v47, v43, v47 dst_sel:DWORD dst_unused:UNUSED_PAD src0_sel:DWORD src1_sel:WORD_1
	global_store_dwordx2 v[48:49], v[46:47], off
	s_branch .LBB0_2231
